# speedup vs baseline: 1.0721x; 1.0061x over previous
.LBB2_24:
	s_or_b64 exec, exec, s[0:1]
	v_and_b32_e32 v1, 31, v0
	v_lshlrev_b32_e32 v2, 2, v1
	v_lshl_or_b32 v2, s10, 7, v2
	v_or_b32_e32 v2, 0x1ee00, v2
	v_lshrrev_b32_e32 v158, 5, v156
	s_waitcnt lgkmcnt(0)
	s_barrier
	s_barrier
	ds_read_b32 v157, v2
	v_mul_u32_u24_e32 v2, 0x88, v1
	s_mul_i32 s0, s11, 0x4400
	v_lshlrev_b32_e32 v2, 1, v2
	v_lshlrev_b32_e32 v3, 4, v158
	v_mov_b32_e32 v138, v0
	v_add3_u32 v159, s0, v2, v3
	ds_read_b128 v[2:5], v159
	ds_read_b128 v[18:21], v159 offset:8704
	ds_read_b128 v[130:133], v159 offset:32
	s_waitcnt vmcnt(10) lgkmcnt(2)
	v_mfma_f32_32x32x16_f16 v[50:65], v[2:5], v[126:129], 0
	s_mov_b32 s4, 0xc060c00
	s_mov_b32 s5, 0xe400
	s_mulk_i32 s11, 0x2400
	s_lshl_b32 s0, s10, 6
	s_or_b32 s0, s11, s0
	s_add_i32 s0, s0, 0x11000
	v_lshl_or_b32 v1, v1, 1, s0
	s_waitcnt lgkmcnt(1)
	v_mfma_f32_32x32x16_f16 v[34:49], v[18:21], v[126:129], 0
	s_or_b32 s0, s8, 2
	s_ashr_i32 s1, s0, 31
	s_lshl_b64 s[0:1], s[0:1], 12
	s_add_u32 s0, s2, s0
	s_addc_u32 s1, s3, s1
	v_cmp_gt_u32_e32 vcc, 32, v156
	v_mfma_f32_32x32x16_f16 v[2:17], v[2:5], v[122:125], 0
	v_mfma_f32_32x32x16_f16 v[18:33], v[18:21], v[122:125], 0
	ds_read_b128 v[134:137], v159 offset:8736
	ds_read_b128 v[160:163], v159 offset:64
	s_waitcnt vmcnt(8) lgkmcnt(2)
	v_mfma_f32_32x32x16_f16 v[50:65], v[130:133], v[118:121], v[50:65]
	s_waitcnt lgkmcnt(1)
	v_mfma_f32_32x32x16_f16 v[34:49], v[134:137], v[118:121], v[34:49]
	v_mfma_f32_32x32x16_f16 v[2:17], v[130:133], v[114:117], v[2:17]
	v_mfma_f32_32x32x16_f16 v[18:33], v[134:137], v[114:117], v[18:33]
	ds_read_b128 v[130:133], v159 offset:8768
	ds_read_b128 v[134:137], v159 offset:96
	s_waitcnt vmcnt(6) lgkmcnt(2)
	v_mfma_f32_32x32x16_f16 v[50:65], v[160:163], v[110:113], v[50:65]
	s_waitcnt lgkmcnt(1)
	v_mfma_f32_32x32x16_f16 v[34:49], v[130:133], v[110:113], v[34:49]
	v_mfma_f32_32x32x16_f16 v[2:17], v[160:163], v[106:109], v[2:17]
	v_mfma_f32_32x32x16_f16 v[18:33], v[130:133], v[106:109], v[18:33]
	ds_read_b128 v[130:133], v159 offset:8800
	ds_read_b128 v[160:163], v159 offset:128
	s_waitcnt vmcnt(4) lgkmcnt(2)
	v_mfma_f32_32x32x16_f16 v[50:65], v[134:137], v[102:105], v[50:65]
	s_waitcnt lgkmcnt(1)
	v_mfma_f32_32x32x16_f16 v[34:49], v[130:133], v[102:105], v[34:49]
	v_mfma_f32_32x32x16_f16 v[2:17], v[134:137], v[98:101], v[2:17]
	v_mfma_f32_32x32x16_f16 v[18:33], v[130:133], v[98:101], v[18:33]
	ds_read_b128 v[130:133], v159 offset:8832
	ds_read_b128 v[134:137], v159 offset:160
	s_waitcnt vmcnt(3) lgkmcnt(2)
	v_mfma_f32_32x32x16_f16 v[50:65], v[160:163], v[94:97], v[50:65]
	s_waitcnt lgkmcnt(1)
	v_mfma_f32_32x32x16_f16 v[34:49], v[130:133], v[94:97], v[34:49]
	v_mfma_f32_32x32x16_f16 v[2:17], v[160:163], v[86:89], v[2:17]
	v_mfma_f32_32x32x16_f16 v[18:33], v[130:133], v[86:89], v[18:33]
	ds_read_b128 v[130:133], v159 offset:8864
	ds_read_b128 v[160:163], v159 offset:192
	s_waitcnt vmcnt(2) lgkmcnt(2)
	v_mfma_f32_32x32x16_f16 v[50:65], v[134:137], v[90:93], v[50:65]
	s_waitcnt lgkmcnt(1)
	v_mfma_f32_32x32x16_f16 v[34:49], v[130:133], v[90:93], v[34:49]
	v_mfma_f32_32x32x16_f16 v[2:17], v[134:137], v[78:81], v[2:17]
	v_mfma_f32_32x32x16_f16 v[18:33], v[130:133], v[78:81], v[18:33]
	ds_read_b128 v[130:133], v159 offset:8896
	ds_read_b128 v[164:167], v159 offset:224
	s_waitcnt vmcnt(1) lgkmcnt(2)
	v_mfma_f32_32x32x16_f16 v[50:65], v[160:163], v[82:85], v[50:65]
	s_waitcnt lgkmcnt(1)
	v_mfma_f32_32x32x16_f16 v[34:49], v[130:133], v[82:85], v[34:49]
	v_mfma_f32_32x32x16_f16 v[2:17], v[160:163], v[70:73], v[2:17]
	v_mfma_f32_32x32x16_f16 v[18:33], v[130:133], v[70:73], v[18:33]
	v_lshlrev_b32_e32 v130, 3, v138
	v_and_b32_e32 v168, 0x1f8, v130
	global_load_dwordx2 v[138:139], v168, s[0:1]
	global_load_dwordx2 v[134:135], v168, s[0:1] offset:512
	global_load_dwordx2 v[132:133], v168, s[0:1] offset:1024
	global_load_dwordx2 v[130:131], v168, s[0:1] offset:1536
	global_load_dwordx2 v[136:137], v168, s[0:1] offset:2048
	s_waitcnt vmcnt(5) lgkmcnt(0)
	v_mfma_f32_32x32x16_f16 v[50:65], v[164:167], v[74:77], v[50:65]
	v_mfma_f32_32x32x16_f16 v[2:17], v[164:167], v[66:69], v[2:17]
	s_nop 10
	v_cvt_pk_f16_f32 v57, v56, v57
	v_cvt_pk_f16_f32 v56, v54, v55
	v_cvt_pk_f16_f32 v55, v52, v53
	v_cvt_pk_f16_f32 v54, v50, v51
	v_perm_b32 v50, v240, v154, s42
	v_perm_b32 v51, v240, v154, s43
	v_perm_b32 v52, v240, v155, s42
	v_perm_b32 v53, v240, v155, s43
	v_pk_add_f16 v50, v50, s5 op_sel_hi:[1,0]
	v_pk_add_f16 v51, v51, s5 op_sel_hi:[1,0]
	v_pk_add_f16 v52, v52, s5 op_sel_hi:[1,0]
	v_pk_add_f16 v53, v53, s5 op_sel_hi:[1,0]
	v_cvt_pk_f16_f32 v65, v64, v65
	v_cvt_pk_f16_f32 v64, v62, v63
	v_cvt_pk_f16_f32 v63, v60, v61
	v_cvt_pk_f16_f32 v62, v58, v59
	v_mfma_f32_32x32x16_f16 v[2:17], v[50:53], v[54:57], v[2:17]
	v_perm_b32 v58, v240, v150, s42
	v_perm_b32 v59, v240, v150, s43
	v_perm_b32 v60, v240, v151, s42
	v_perm_b32 v61, v240, v151, s43
	v_pk_add_f16 v58, v58, s5 op_sel_hi:[1,0]
	v_pk_add_f16 v59, v59, s5 op_sel_hi:[1,0]
	v_pk_add_f16 v60, v60, s5 op_sel_hi:[1,0]
	v_pk_add_f16 v61, v61, s5 op_sel_hi:[1,0]
	s_nop 1
	v_mfma_f32_32x32x16_f16 v[2:17], v[58:61], v[62:65], v[2:17]
	ds_read_b128 v[160:163], v159 offset:8928
	v_perm_b32 v155, v240, v152, s43
	v_perm_b32 v164, v240, v153, s42
	s_waitcnt lgkmcnt(0)
	v_mfma_f32_32x32x16_f16 v[18:33], v[160:163], v[66:69], v[18:33]
	v_perm_b32 v154, v240, v152, s42
	v_perm_b32 v165, v240, v153, s43
	v_pk_add_f16 v152, v154, s5 op_sel_hi:[1,0]
	v_pk_add_f16 v153, v155, s5 op_sel_hi:[1,0]
	v_pk_add_f16 v154, v164, s5 op_sel_hi:[1,0]
	v_pk_add_f16 v155, v165, s5 op_sel_hi:[1,0]
	v_mfma_f32_32x32x16_f16 v[34:49], v[160:163], v[74:77], v[34:49]
	v_perm_b32 v151, v240, v148, s43
	v_perm_b32 v164, v240, v149, s42
	v_mfma_f32_32x32x16_f16 v[18:33], v[152:155], v[54:57], v[18:33]
	v_perm_b32 v150, v240, v148, s42
	v_perm_b32 v165, v240, v149, s43
	v_pk_add_f16 v148, v150, s5 op_sel_hi:[1,0]
	v_pk_add_f16 v149, v151, s5 op_sel_hi:[1,0]
	v_pk_add_f16 v150, v164, s5 op_sel_hi:[1,0]
	v_pk_add_f16 v151, v165, s5 op_sel_hi:[1,0]
	s_nop 2
	v_cvt_pk_f16_f32 v41, v40, v41
	v_cvt_pk_f16_f32 v40, v38, v39
	v_cvt_pk_f16_f32 v38, v34, v35
	v_cvt_pk_f16_f32 v39, v36, v37
	v_mfma_f32_32x32x16_f16 v[18:33], v[148:151], v[62:65], v[18:33]
	v_perm_b32 v34, v240, v146, s42
	v_perm_b32 v35, v240, v146, s43
	v_perm_b32 v36, v240, v147, s42
	v_perm_b32 v37, v240, v147, s43
	v_pk_add_f16 v34, v34, s5 op_sel_hi:[1,0]
	v_pk_add_f16 v35, v35, s5 op_sel_hi:[1,0]
	v_pk_add_f16 v36, v36, s5 op_sel_hi:[1,0]
	v_pk_add_f16 v37, v37, s5 op_sel_hi:[1,0]
	v_perm_b32 v146, v240, v144, s42
	v_perm_b32 v144, v240, v144, s43
	v_perm_b32 v147, v240, v145, s42
	v_perm_b32 v53, v240, v145, s43
	v_pk_add_f16 v50, v146, s5 op_sel_hi:[1,0]
	v_pk_add_f16 v51, v144, s5 op_sel_hi:[1,0]
	v_pk_add_f16 v52, v147, s5 op_sel_hi:[1,0]
	v_pk_add_f16 v53, v53, s5 op_sel_hi:[1,0]
	v_cvt_pk_f16_f32 v49, v48, v49
	v_cvt_pk_f16_f32 v48, v46, v47
	v_cvt_pk_f16_f32 v47, v44, v45
	v_mfma_f32_32x32x16_f16 v[2:17], v[34:37], v[38:41], v[2:17]
	v_cvt_pk_f16_f32 v46, v42, v43
	v_lshlrev_b32_e32 v54, 8, v140
	v_mfma_f32_32x32x16_f16 v[18:33], v[50:53], v[38:41], v[18:33]
	v_lshrrev_b32_e32 v37, 16, v141
	v_lshrrev_b32_e32 v38, 8, v141
	v_perm_b32 v34, v54, v140, s4
	v_perm_b32 v37, v38, v37, s4
	v_or_b32_e32 v34, 0x64006400, v34
	v_perm_b32 v35, v240, v140, s43
	v_perm_b32 v36, v240, v141, s42
	v_or_b32_e32 v37, 0x64006400, v37
	v_perm_b32 v42, v240, v142, s42
	v_perm_b32 v43, v240, v142, s43
	v_perm_b32 v44, v240, v143, s42
	v_perm_b32 v45, v240, v143, s43
	v_pk_add_f16 v34, v34, s5 op_sel_hi:[1,0]
	v_pk_add_f16 v35, v35, s5 op_sel_hi:[1,0]
	v_pk_add_f16 v36, v36, s5 op_sel_hi:[1,0]
	v_pk_add_f16 v37, v37, s5 op_sel_hi:[1,0]
	v_pk_add_f16 v42, v42, s5 op_sel_hi:[1,0]
	v_pk_add_f16 v43, v43, s5 op_sel_hi:[1,0]
	v_pk_add_f16 v44, v44, s5 op_sel_hi:[1,0]
	v_pk_add_f16 v45, v45, s5 op_sel_hi:[1,0]
	v_mfma_f32_32x32x16_f16 v[18:33], v[34:37], v[46:49], v[18:33]
	global_load_dwordx2 v[154:155], v168, s[0:1] offset:2560
	global_load_dwordx2 v[152:153], v168, s[0:1] offset:3072
	global_load_dwordx2 v[150:151], v168, s[0:1] offset:3584
	v_mov_b32_e32 v148, v0
	s_or_b32 s0, s8, 4
	s_ashr_i32 s1, s0, 31
	s_lshl_b64 s[0:1], s[0:1], 12
	v_mfma_f32_32x32x16_f16 v[2:17], v[42:45], v[46:49], v[2:17]
	s_nop 3
	v_add_f32_e32 v196, v157, v18
	v_mul_u32_u24_e32 v18, 0x120, v158
	v_lshl_add_u32 v158, v18, 1, v1
	v_cvt_f16_f32_e32 v1, v196
	v_add_f32_e32 v204, v157, v20
	v_add_f32_e32 v160, v157, v21
	v_add_f32_e32 v162, v157, v22
	s_nop 0
	v_add_f32_e32 v193, v157, v2
	v_add_f32_e32 v198, v157, v3
	v_cvt_pk_f16_f32 v2, v193, v198
	ds_write_b16 v158, v1 offset:4608
	v_add_f32_e32 v203, v157, v4
	v_add_f32_e32 v1, v157, v5
	ds_write_b16 v158, v2
	ds_write_b16_d16_hi v158, v2 offset:144
	v_cvt_pk_f16_f32 v2, v203, v204
	v_cvt_pk_f16_f32 v4, v1, v160
	v_add_f32_e32 v161, v157, v6
	v_add_f32_e32 v163, v157, v7
	v_add_f32_e32 v164, v157, v23
	ds_write_b16 v158, v2 offset:288
	ds_write_b16_d16_hi v158, v2 offset:4896
	ds_write_b16 v158, v4 offset:432
	ds_write_b16_d16_hi v158, v4 offset:5040
	v_cvt_pk_f16_f32 v2, v161, v162
	v_cvt_pk_f16_f32 v4, v163, v164
	v_add_f32_e32 v165, v157, v8
	v_add_f32_e32 v166, v157, v24
	v_add_f32_e32 v167, v157, v9
	v_add_f32_e32 v168, v157, v25
	ds_write_b16 v158, v2 offset:1152
	ds_write_b16_d16_hi v158, v2 offset:5760
	ds_write_b16 v158, v4 offset:1296
	ds_write_b16_d16_hi v158, v4 offset:5904
	v_cvt_pk_f16_f32 v2, v165, v166
	v_cvt_pk_f16_f32 v4, v167, v168
	v_add_f32_e32 v169, v157, v10
	v_add_f32_e32 v170, v157, v26
	v_add_f32_e32 v171, v157, v11
	v_add_f32_e32 v172, v157, v27
	ds_write_b16 v158, v2 offset:1440
	ds_write_b16_d16_hi v158, v2 offset:6048
	ds_write_b16 v158, v4 offset:1584
	ds_write_b16_d16_hi v158, v4 offset:6192
	v_cvt_pk_f16_f32 v2, v169, v170
	v_cvt_pk_f16_f32 v4, v171, v172
	v_add_f32_e32 v173, v157, v12
	v_add_f32_e32 v174, v157, v28
	v_add_f32_e32 v175, v157, v13
	v_add_f32_e32 v176, v157, v29
	ds_write_b16 v158, v2 offset:2304
	ds_write_b16_d16_hi v158, v2 offset:6912
	ds_write_b16 v158, v4 offset:2448
	ds_write_b16_d16_hi v158, v4 offset:7056
	v_cvt_pk_f16_f32 v2, v173, v174
	v_cvt_pk_f16_f32 v4, v175, v176
	v_add_f32_e32 v177, v157, v14
	v_add_f32_e32 v178, v157, v30
	v_add_f32_e32 v179, v157, v15
	v_add_f32_e32 v180, v157, v31
	ds_write_b16 v158, v2 offset:2592
	ds_write_b16_d16_hi v158, v2 offset:7200
	ds_write_b16 v158, v4 offset:2736
	ds_write_b16_d16_hi v158, v4 offset:7344
	v_cvt_pk_f16_f32 v2, v177, v178
	v_cvt_pk_f16_f32 v4, v179, v180
	v_add_f32_e32 v200, v157, v19
	v_add_f32_e32 v181, v157, v16
	v_add_f32_e32 v183, v157, v32
	v_add_f32_e32 v182, v157, v17
	v_add_f32_e32 v184, v157, v33
	v_cvt_pk_f16_f32 v18, v200, v181
	ds_write_b16 v158, v2 offset:3456
	ds_write_b16_d16_hi v158, v2 offset:8064
	ds_write_b16 v158, v4 offset:3600
	ds_write_b16_d16_hi v158, v4 offset:8208
	v_cvt_pk_f16_f32 v3, v183, v182
	v_cvt_f16_f32_e32 v5, v184
	ds_write_b16 v158, v18 offset:4752
	ds_write_b16_d16_hi v158, v18 offset:3744
	ds_write_b16 v158, v3 offset:8352
	ds_write_b16_d16_hi v158, v3 offset:3888
	ds_write_b16 v158, v5 offset:8496
	s_waitcnt lgkmcnt(0)
	s_barrier
	ds_read_b128 v[2:5], v159 offset:34816
	ds_read_b128 v[18:21], v159 offset:43520
	ds_read_b128 v[140:143], v159 offset:34848
	ds_read_b128 v[144:147], v159 offset:43552
	s_waitcnt lgkmcnt(3)
	v_mfma_f32_32x32x16_f16 v[50:65], v[2:5], v[126:129], 0
	s_add_u32 s0, s2, s0
	s_addc_u32 s1, s3, s1
	s_waitcnt lgkmcnt(2)
	v_mfma_f32_32x32x16_f16 v[34:49], v[18:21], v[126:129], 0
	v_mfma_f32_32x32x16_f16 v[2:17], v[2:5], v[122:125], 0
	v_mfma_f32_32x32x16_f16 v[18:33], v[18:21], v[122:125], 0
	ds_read_b128 v[242:245], v159 offset:34880
	ds_read_b128 v[246:249], v159 offset:43584
	s_waitcnt lgkmcnt(3)
	v_mfma_f32_32x32x16_f16 v[50:65], v[140:143], v[118:121], v[50:65]
	s_waitcnt lgkmcnt(2)
	v_mfma_f32_32x32x16_f16 v[34:49], v[144:147], v[118:121], v[34:49]
	v_mfma_f32_32x32x16_f16 v[2:17], v[140:143], v[114:117], v[2:17]
	v_mfma_f32_32x32x16_f16 v[18:33], v[144:147], v[114:117], v[18:33]
	ds_read_b128 v[140:143], v159 offset:34912
	ds_read_b128 v[144:147], v159 offset:43616
	s_waitcnt lgkmcnt(3)
	v_mfma_f32_32x32x16_f16 v[50:65], v[242:245], v[110:113], v[50:65]
	s_waitcnt lgkmcnt(2)
	v_mfma_f32_32x32x16_f16 v[34:49], v[246:249], v[110:113], v[34:49]
	v_mfma_f32_32x32x16_f16 v[2:17], v[242:245], v[106:109], v[2:17]
	v_mfma_f32_32x32x16_f16 v[18:33], v[246:249], v[106:109], v[18:33]
	ds_read_b128 v[242:245], v159 offset:34944
	ds_read_b128 v[246:249], v159 offset:43648
	s_waitcnt lgkmcnt(3)
	v_mfma_f32_32x32x16_f16 v[50:65], v[140:143], v[102:105], v[50:65]
	s_waitcnt lgkmcnt(2)
	v_mfma_f32_32x32x16_f16 v[34:49], v[144:147], v[102:105], v[34:49]
	v_mfma_f32_32x32x16_f16 v[2:17], v[140:143], v[98:101], v[2:17]
	v_mfma_f32_32x32x16_f16 v[18:33], v[144:147], v[98:101], v[18:33]
	ds_read_b128 v[186:189], v159 offset:34976
	ds_read_b128 v[206:209], v159 offset:43680
	s_waitcnt lgkmcnt(3)
	v_mfma_f32_32x32x16_f16 v[50:65], v[242:245], v[94:97], v[50:65]
	s_waitcnt lgkmcnt(2)
	v_mfma_f32_32x32x16_f16 v[34:49], v[246:249], v[94:97], v[34:49]
	v_mfma_f32_32x32x16_f16 v[2:17], v[242:245], v[86:89], v[2:17]
	v_mfma_f32_32x32x16_f16 v[18:33], v[246:249], v[86:89], v[18:33]
	ds_read_b128 v[140:143], v159 offset:35008
	ds_read_b128 v[144:147], v159 offset:43712
	s_waitcnt lgkmcnt(3)
	v_mfma_f32_32x32x16_f16 v[50:65], v[186:189], v[90:93], v[50:65]
	s_waitcnt lgkmcnt(2)
	v_mfma_f32_32x32x16_f16 v[34:49], v[206:209], v[90:93], v[34:49]
	v_mfma_f32_32x32x16_f16 v[2:17], v[186:189], v[78:81], v[2:17]
	v_mfma_f32_32x32x16_f16 v[18:33], v[206:209], v[78:81], v[18:33]
	ds_read_b128 v[186:189], v159 offset:35040
	ds_read_b128 v[206:209], v159 offset:43744
	s_waitcnt lgkmcnt(3)
	v_mfma_f32_32x32x16_f16 v[50:65], v[140:143], v[82:85], v[50:65]
	s_waitcnt lgkmcnt(2)
	v_mfma_f32_32x32x16_f16 v[34:49], v[144:147], v[82:85], v[34:49]
	v_mfma_f32_32x32x16_f16 v[2:17], v[140:143], v[70:73], v[2:17]
	v_lshlrev_b32_e32 v140, 3, v148
	v_and_b32_e32 v185, 0x1f8, v140
	global_load_dwordx2 v[148:149], v185, s[0:1]
	global_load_dwordx2 v[142:143], v185, s[0:1] offset:1024
	global_load_dwordx2 v[140:141], v185, s[0:1] offset:1536
	v_mfma_f32_32x32x16_f16 v[18:33], v[144:147], v[70:73], v[18:33]
	global_load_dwordx2 v[144:145], v185, s[0:1] offset:512
	global_load_dwordx2 v[146:147], v185, s[0:1] offset:2048
	s_waitcnt lgkmcnt(1)
	v_mfma_f32_32x32x16_f16 v[50:65], v[186:189], v[74:77], v[50:65]
	v_mfma_f32_32x32x16_f16 v[2:17], v[186:189], v[66:69], v[2:17]
	s_nop 10
	v_cvt_pk_f16_f32 v57, v56, v57
	v_cvt_pk_f16_f32 v56, v54, v55
	v_cvt_pk_f16_f32 v54, v50, v51
	s_waitcnt vmcnt(12)
	v_cvt_pk_f16_f32 v55, v52, v53
	s_waitcnt vmcnt(8)
	v_perm_b32 v50, v240, v138, s42
	v_perm_b32 v51, v240, v138, s43
	v_perm_b32 v52, v240, v139, s42
	v_perm_b32 v53, v240, v139, s43
	v_perm_b32 v139, v240, v136, s43
	v_pk_add_f16 v50, v50, s5 op_sel_hi:[1,0]
	v_pk_add_f16 v51, v51, s5 op_sel_hi:[1,0]
	v_pk_add_f16 v52, v52, s5 op_sel_hi:[1,0]
	v_pk_add_f16 v53, v53, s5 op_sel_hi:[1,0]
	v_perm_b32 v190, v240, v137, s42
	s_waitcnt lgkmcnt(0)
	v_mfma_f32_32x32x16_f16 v[18:33], v[206:209], v[66:69], v[18:33]
	v_perm_b32 v138, v240, v136, s42
	v_perm_b32 v191, v240, v137, s43
	v_pk_add_f16 v136, v138, s5 op_sel_hi:[1,0]
	v_pk_add_f16 v137, v139, s5 op_sel_hi:[1,0]
	v_pk_add_f16 v138, v190, s5 op_sel_hi:[1,0]
	v_pk_add_f16 v139, v191, s5 op_sel_hi:[1,0]
	v_cvt_pk_f16_f32 v65, v64, v65
	v_cvt_pk_f16_f32 v64, v62, v63
	v_cvt_pk_f16_f32 v63, v60, v61
	v_cvt_pk_f16_f32 v62, v58, v59
	v_mfma_f32_32x32x16_f16 v[34:49], v[206:209], v[74:77], v[34:49]
	v_mfma_f32_32x32x16_f16 v[2:17], v[50:53], v[54:57], v[2:17]
	s_waitcnt vmcnt(7)
	v_perm_b32 v58, v240, v134, s42
	v_perm_b32 v59, v240, v134, s43
	v_perm_b32 v60, v240, v135, s42
	v_perm_b32 v61, v240, v135, s43
	v_pk_add_f16 v58, v58, s5 op_sel_hi:[1,0]
	v_pk_add_f16 v59, v59, s5 op_sel_hi:[1,0]
	v_pk_add_f16 v60, v60, s5 op_sel_hi:[1,0]
	v_pk_add_f16 v61, v61, s5 op_sel_hi:[1,0]
	v_mfma_f32_32x32x16_f16 v[18:33], v[136:139], v[54:57], v[18:33]
	v_perm_b32 v134, v240, v154, s42
	v_perm_b32 v135, v240, v154, s43
	v_perm_b32 v154, v240, v155, s42
	v_perm_b32 v155, v240, v155, s43
	v_pk_add_f16 v210, v134, s5 op_sel_hi:[1,0]
	v_pk_add_f16 v211, v135, s5 op_sel_hi:[1,0]
	v_pk_add_f16 v212, v154, s5 op_sel_hi:[1,0]
	v_pk_add_f16 v213, v155, s5 op_sel_hi:[1,0]
	v_cvt_pk_f16_f32 v41, v40, v41
	v_cvt_pk_f16_f32 v40, v38, v39
	v_cvt_pk_f16_f32 v39, v36, v37
	v_cvt_pk_f16_f32 v38, v34, v35
	v_mfma_f32_32x32x16_f16 v[2:17], v[58:61], v[62:65], v[2:17]
	v_perm_b32 v34, v240, v132, s42
	v_perm_b32 v35, v240, v132, s43
	v_perm_b32 v36, v240, v133, s42
	v_perm_b32 v37, v240, v133, s43
	v_pk_add_f16 v34, v34, s5 op_sel_hi:[1,0]
	v_pk_add_f16 v35, v35, s5 op_sel_hi:[1,0]
	v_pk_add_f16 v36, v36, s5 op_sel_hi:[1,0]
	v_pk_add_f16 v37, v37, s5 op_sel_hi:[1,0]
	s_waitcnt vmcnt(6)
	v_mfma_f32_32x32x16_f16 v[18:33], v[210:213], v[62:65], v[18:33]
	v_perm_b32 v132, v240, v152, s42
	v_perm_b32 v133, v240, v152, s43
	v_perm_b32 v134, v240, v153, s42
	v_perm_b32 v53, v240, v153, s43
	v_pk_add_f16 v50, v132, s5 op_sel_hi:[1,0]
	v_pk_add_f16 v51, v133, s5 op_sel_hi:[1,0]
	v_pk_add_f16 v52, v134, s5 op_sel_hi:[1,0]
	v_pk_add_f16 v53, v53, s5 op_sel_hi:[1,0]
	v_cvt_pk_f16_f32 v49, v48, v49
	v_cvt_pk_f16_f32 v48, v46, v47
	v_cvt_pk_f16_f32 v47, v44, v45
	v_cvt_pk_f16_f32 v46, v42, v43
	v_mfma_f32_32x32x16_f16 v[2:17], v[34:37], v[38:41], v[2:17]
	v_perm_b32 v42, v240, v130, s42
	v_perm_b32 v43, v240, v130, s43
	v_perm_b32 v44, v240, v131, s42
	v_perm_b32 v45, v240, v131, s43
	v_pk_add_f16 v42, v42, s5 op_sel_hi:[1,0]
	v_pk_add_f16 v43, v43, s5 op_sel_hi:[1,0]
	v_pk_add_f16 v44, v44, s5 op_sel_hi:[1,0]
	v_pk_add_f16 v45, v45, s5 op_sel_hi:[1,0]
	s_waitcnt vmcnt(5)
	v_lshlrev_b32_e32 v54, 8, v150
	v_mfma_f32_32x32x16_f16 v[18:33], v[50:53], v[38:41], v[18:33]
	v_lshrrev_b32_e32 v37, 16, v151
	v_lshrrev_b32_e32 v38, 8, v151
	v_perm_b32 v34, v54, v150, s4
	v_perm_b32 v37, v38, v37, s4
	v_or_b32_e32 v34, 0x64006400, v34
	v_perm_b32 v35, v240, v150, s43
	v_perm_b32 v36, v240, v151, s42
	v_or_b32_e32 v37, 0x64006400, v37
	v_pk_add_f16 v34, v34, s5 op_sel_hi:[1,0]
	v_pk_add_f16 v35, v35, s5 op_sel_hi:[1,0]
	v_pk_add_f16 v36, v36, s5 op_sel_hi:[1,0]
	v_pk_add_f16 v37, v37, s5 op_sel_hi:[1,0]
	v_mfma_f32_32x32x16_f16 v[2:17], v[42:45], v[46:49], v[2:17]
	global_load_dwordx2 v[154:155], v185, s[0:1] offset:2560
	global_load_dwordx2 v[152:153], v185, s[0:1] offset:3072
	global_load_dwordx2 v[150:151], v185, s[0:1] offset:3584
	s_or_b32 s0, s8, 6
	s_ashr_i32 s1, s0, 31
	s_lshl_b64 s[0:1], s[0:1], 12
	s_add_u32 s0, s2, s0
	v_mfma_f32_32x32x16_f16 v[18:33], v[34:37], v[46:49], v[18:33]
	s_nop 3
	v_add_f32_e32 v185, v157, v2
	v_add_f32_e32 v187, v157, v3
	v_cvt_pk_f16_f32 v2, v185, v187
	v_add_f32_e32 v189, v157, v4
	v_add_f32_e32 v191, v157, v5
	ds_write_b16 v158, v2 offset:18432
	s_nop 0
	s_nop 0
	v_add_f32_e32 v190, v157, v20
	v_add_f32_e32 v192, v157, v21
	ds_write_b16_d16_hi v158, v2 offset:18576
	v_cvt_pk_f16_f32 v2, v189, v190
	v_cvt_pk_f16_f32 v4, v191, v192
	v_add_f32_e32 v194, v157, v6
	v_add_f32_e32 v195, v157, v22
	v_add_f32_e32 v197, v157, v7
	v_add_f32_e32 v199, v157, v23
	ds_write_b16 v158, v2 offset:18720
	ds_write_b16_d16_hi v158, v2 offset:23328
	ds_write_b16 v158, v4 offset:18864
	ds_write_b16_d16_hi v158, v4 offset:23472
	v_cvt_pk_f16_f32 v2, v194, v195
	v_cvt_pk_f16_f32 v4, v197, v199
	v_add_f32_e32 v201, v157, v8
	v_add_f32_e32 v202, v157, v24
	v_add_f32_e32 v205, v157, v9
	v_add_f32_e32 v206, v157, v25
	ds_write_b16 v158, v2 offset:19584
	ds_write_b16_d16_hi v158, v2 offset:24192
	ds_write_b16 v158, v4 offset:19728
	ds_write_b16_d16_hi v158, v4 offset:24336
	v_cvt_pk_f16_f32 v2, v201, v202
	v_cvt_pk_f16_f32 v4, v205, v206
	v_add_f32_e32 v207, v157, v10
	v_add_f32_e32 v209, v157, v26
	v_add_f32_e32 v208, v157, v11
	v_add_f32_e32 v210, v157, v27
	ds_write_b16 v158, v2 offset:19872
	ds_write_b16_d16_hi v158, v2 offset:24480
	ds_write_b16 v158, v4 offset:20016
	ds_write_b16_d16_hi v158, v4 offset:24624
	v_cvt_pk_f16_f32 v2, v207, v209
	v_cvt_pk_f16_f32 v4, v208, v210
	v_add_f32_e32 v211, v157, v12
	v_add_f32_e32 v212, v157, v28
	v_add_f32_e32 v213, v157, v13
	v_add_f32_e32 v214, v157, v29
	ds_write_b16 v158, v2 offset:20736
	ds_write_b16_d16_hi v158, v2 offset:25344
	ds_write_b16 v158, v4 offset:20880
	ds_write_b16_d16_hi v158, v4 offset:25488
	v_cvt_pk_f16_f32 v2, v211, v212
	v_cvt_pk_f16_f32 v4, v213, v214
	v_add_f32_e32 v215, v157, v14
	v_add_f32_e32 v216, v157, v30
	v_add_f32_e32 v217, v157, v15
	v_add_f32_e32 v218, v157, v31
	ds_write_b16 v158, v2 offset:21024
	ds_write_b16_d16_hi v158, v2 offset:25632
	ds_write_b16 v158, v4 offset:21168
	ds_write_b16_d16_hi v158, v4 offset:25776
	v_cvt_pk_f16_f32 v2, v215, v216
	v_cvt_pk_f16_f32 v4, v217, v218
	v_add_f32_e32 v186, v157, v18
	v_add_f32_e32 v188, v157, v19
	v_add_f32_e32 v219, v157, v16
	v_add_f32_e32 v221, v157, v32
	v_add_f32_e32 v220, v157, v17
	v_add_f32_e32 v222, v157, v33
	v_cvt_pk_f16_f32 v18, v186, v188
	ds_write_b16 v158, v2 offset:21888
	ds_write_b16_d16_hi v158, v2 offset:26496
	ds_write_b16 v158, v4 offset:22032
	ds_write_b16_d16_hi v158, v4 offset:26640
	v_cvt_pk_f16_f32 v2, v219, v221
	v_cvt_pk_f16_f32 v4, v220, v222
	ds_write_b16 v158, v18 offset:23040
	ds_write_b16_d16_hi v158, v18 offset:23184
	ds_write_b16 v158, v2 offset:22176
	ds_write_b16_d16_hi v158, v2 offset:26784
	ds_write_b16 v158, v4 offset:22320
	ds_write_b16_d16_hi v158, v4 offset:26928
	s_waitcnt lgkmcnt(0)
	s_barrier
	ds_read_b128 v[2:5], v159
	ds_read_b128 v[18:21], v159 offset:8704
	s_waitcnt lgkmcnt(1)
	v_mfma_f32_32x32x16_f16 v[50:65], v[2:5], v[126:129], 0
	v_lshlrev_b32_e32 v0, 3, v0
	s_addc_u32 s1, s3, s1
	v_and_b32_e32 v0, 0x1f8, v0
	global_load_dwordx2 v[138:139], v0, s[0:1]
	s_waitcnt lgkmcnt(0)
	v_mfma_f32_32x32x16_f16 v[34:49], v[18:21], v[126:129], 0
	v_mfma_f32_32x32x16_f16 v[2:17], v[2:5], v[122:125], 0
	v_mfma_f32_32x32x16_f16 v[18:33], v[18:21], v[122:125], 0
	ds_read_b128 v[130:133], v159 offset:32
	ds_read_b128 v[134:137], v159 offset:8736
	s_waitcnt lgkmcnt(1)
	v_mfma_f32_32x32x16_f16 v[50:65], v[130:133], v[118:121], v[50:65]
	s_waitcnt lgkmcnt(0)
	v_mfma_f32_32x32x16_f16 v[34:49], v[134:137], v[118:121], v[34:49]
	v_mfma_f32_32x32x16_f16 v[2:17], v[130:133], v[114:117], v[2:17]
	v_mfma_f32_32x32x16_f16 v[18:33], v[134:137], v[114:117], v[18:33]
	ds_read_b128 v[224:227], v159 offset:64
	ds_read_b128 v[228:231], v159 offset:8768
	ds_read_b128 v[130:133], v159 offset:96
	ds_read_b128 v[134:137], v159 offset:8800
	s_waitcnt lgkmcnt(3)
	v_mfma_f32_32x32x16_f16 v[50:65], v[224:227], v[110:113], v[50:65]
	s_waitcnt lgkmcnt(2)
	v_mfma_f32_32x32x16_f16 v[34:49], v[228:231], v[110:113], v[34:49]
	v_mfma_f32_32x32x16_f16 v[2:17], v[224:227], v[106:109], v[2:17]
	v_mfma_f32_32x32x16_f16 v[18:33], v[228:231], v[106:109], v[18:33]
	ds_read_b128 v[224:227], v159 offset:128
	ds_read_b128 v[228:231], v159 offset:8832
	s_waitcnt lgkmcnt(3)
	v_mfma_f32_32x32x16_f16 v[50:65], v[130:133], v[102:105], v[50:65]
	s_waitcnt lgkmcnt(2)
	v_mfma_f32_32x32x16_f16 v[34:49], v[134:137], v[102:105], v[34:49]
	v_mfma_f32_32x32x16_f16 v[2:17], v[130:133], v[98:101], v[2:17]
	v_mfma_f32_32x32x16_f16 v[18:33], v[134:137], v[98:101], v[18:33]
	ds_read_b128 v[130:133], v159 offset:160
	ds_read_b128 v[134:137], v159 offset:8864
	s_waitcnt lgkmcnt(3)
	v_mfma_f32_32x32x16_f16 v[50:65], v[224:227], v[94:97], v[50:65]
	s_waitcnt lgkmcnt(2)
	v_mfma_f32_32x32x16_f16 v[34:49], v[228:231], v[94:97], v[34:49]
	v_mfma_f32_32x32x16_f16 v[2:17], v[224:227], v[86:89], v[2:17]
	v_mfma_f32_32x32x16_f16 v[18:33], v[228:231], v[86:89], v[18:33]
	ds_read_b128 v[224:227], v159 offset:192
	ds_read_b128 v[228:231], v159 offset:8896
	s_waitcnt lgkmcnt(3)
	v_mfma_f32_32x32x16_f16 v[50:65], v[130:133], v[90:93], v[50:65]
	s_waitcnt lgkmcnt(2)
	v_mfma_f32_32x32x16_f16 v[34:49], v[134:137], v[90:93], v[34:49]
	v_mfma_f32_32x32x16_f16 v[2:17], v[130:133], v[78:81], v[2:17]
	v_add_f32_e32 v130, v193, v196
	v_add_f32_e32 v130, 0, v130
	v_add_f32_e32 v132, v198, v200
	v_add_f32_e32 v130, v132, v130
	v_mul_f32_e32 v132, v200, v200
	v_fmac_f32_e32 v132, v198, v198
	v_mul_f32_e32 v131, v196, v196
	v_mfma_f32_32x32x16_f16 v[18:33], v[134:137], v[78:81], v[18:33]
	ds_read_b128 v[232:235], v159 offset:224
	ds_read_b128 v[236:239], v159 offset:8928
	v_fmac_f32_e32 v131, v193, v193
	v_add_f32_e32 v131, v131, v132
	v_add_f32_e32 v132, v203, v204
	v_add_f32_e32 v130, v132, v130
	v_mul_f32_e32 v132, v204, v204
	s_waitcnt lgkmcnt(3)
	v_mfma_f32_32x32x16_f16 v[50:65], v[224:227], v[82:85], v[50:65]
	v_fmac_f32_e32 v132, v203, v203
	v_add_f32_e32 v193, v132, v131
	v_add_f32_e32 v131, v1, v160
	v_add_f32_e32 v196, v131, v130
	global_load_dwordx2 v[134:135], v0, s[0:1] offset:512
	global_load_dwordx2 v[132:133], v0, s[0:1] offset:1024
	global_load_dwordx2 v[130:131], v0, s[0:1] offset:1536
	s_waitcnt lgkmcnt(2)
	v_mfma_f32_32x32x16_f16 v[34:49], v[228:231], v[82:85], v[34:49]
	global_load_dwordx2 v[136:137], v0, s[0:1] offset:2048
	v_mfma_f32_32x32x16_f16 v[2:17], v[224:227], v[70:73], v[2:17]
	v_mfma_f32_32x32x16_f16 v[18:33], v[228:231], v[70:73], v[18:33]
	s_waitcnt lgkmcnt(1)
	v_mfma_f32_32x32x16_f16 v[50:65], v[232:235], v[74:77], v[50:65]
	v_mfma_f32_32x32x16_f16 v[2:17], v[232:235], v[66:69], v[2:17]
	s_nop 10
	v_cvt_pk_f16_f32 v57, v56, v57
	v_cvt_pk_f16_f32 v56, v54, v55
	v_cvt_pk_f16_f32 v54, v50, v51
	s_waitcnt vmcnt(12)
	v_lshlrev_b32_e32 v50, 8, v148
	v_cvt_pk_f16_f32 v55, v52, v53
	v_perm_b32 v50, v50, v148, s4
	v_lshrrev_b32_e32 v51, 16, v148
	v_lshrrev_b32_e32 v52, 8, v148
	v_lshrrev_b32_e32 v53, 16, v149
	v_lshrrev_b32_e32 v148, 8, v149
	v_perm_b32 v51, v52, v51, s4
	v_lshlrev_b32_e32 v52, 8, v149
	v_perm_b32 v53, v148, v53, s4
	s_waitcnt vmcnt(8)
	v_perm_b32 v52, v52, v149, s4
	v_perm_b32 v149, v240, v146, s43
	v_perm_b32 v198, v240, v147, s42
	s_waitcnt lgkmcnt(0)
	v_mfma_f32_32x32x16_f16 v[18:33], v[236:239], v[66:69], v[18:33]
	v_or_b32_e32 v50, 0x64006400, v50
	v_or_b32_e32 v51, 0x64006400, v51
	v_or_b32_e32 v52, 0x64006400, v52
	v_or_b32_e32 v53, 0x64006400, v53
	v_pk_add_f16 v50, v50, s5 op_sel_hi:[1,0]
	v_pk_add_f16 v51, v51, s5 op_sel_hi:[1,0]
	v_pk_add_f16 v52, v52, s5 op_sel_hi:[1,0]
	v_pk_add_f16 v53, v53, s5 op_sel_hi:[1,0]
	v_perm_b32 v148, v240, v146, s42
	v_perm_b32 v200, v240, v147, s43
	v_pk_add_f16 v146, v148, s5 op_sel_hi:[1,0]
	v_pk_add_f16 v147, v149, s5 op_sel_hi:[1,0]
	v_pk_add_f16 v148, v198, s5 op_sel_hi:[1,0]
	v_pk_add_f16 v149, v200, s5 op_sel_hi:[1,0]
	v_cvt_pk_f16_f32 v65, v64, v65
	v_cvt_pk_f16_f32 v64, v62, v63
	v_cvt_pk_f16_f32 v62, v58, v59
	v_cvt_pk_f16_f32 v63, v60, v61
	s_waitcnt vmcnt(7)
	v_mfma_f32_32x32x16_f16 v[34:49], v[236:239], v[74:77], v[34:49]
	v_mfma_f32_32x32x16_f16 v[2:17], v[50:53], v[54:57], v[2:17]
	v_perm_b32 v58, v240, v144, s42
	v_perm_b32 v59, v240, v144, s43
	v_perm_b32 v60, v240, v145, s42
	v_perm_b32 v61, v240, v145, s43
	v_mfma_f32_32x32x16_f16 v[18:33], v[146:149], v[54:57], v[18:33]
	v_pk_add_f16 v58, v58, s5 op_sel_hi:[1,0]
	v_pk_add_f16 v59, v59, s5 op_sel_hi:[1,0]
	v_pk_add_f16 v60, v60, s5 op_sel_hi:[1,0]
	v_pk_add_f16 v61, v61, s5 op_sel_hi:[1,0]
	v_perm_b32 v144, v240, v154, s42
	v_perm_b32 v145, v240, v154, s43
	v_perm_b32 v154, v240, v155, s42
	v_perm_b32 v155, v240, v155, s43
	v_pk_add_f16 v224, v144, s5 op_sel_hi:[1,0]
	v_pk_add_f16 v225, v145, s5 op_sel_hi:[1,0]
	v_pk_add_f16 v226, v154, s5 op_sel_hi:[1,0]
	v_pk_add_f16 v227, v155, s5 op_sel_hi:[1,0]
	v_cvt_pk_f16_f32 v41, v40, v41
	v_cvt_pk_f16_f32 v40, v38, v39
	v_cvt_pk_f16_f32 v39, v36, v37
	v_cvt_pk_f16_f32 v38, v34, v35
	s_waitcnt vmcnt(6)
	v_mfma_f32_32x32x16_f16 v[2:17], v[58:61], v[62:65], v[2:17]
	v_perm_b32 v34, v240, v142, s42
	v_perm_b32 v35, v240, v142, s43
	v_mfma_f32_32x32x16_f16 v[18:33], v[224:227], v[62:65], v[18:33]
	v_perm_b32 v36, v240, v143, s42
	v_perm_b32 v37, v240, v143, s43
	v_pk_add_f16 v34, v34, s5 op_sel_hi:[1,0]
	v_pk_add_f16 v35, v35, s5 op_sel_hi:[1,0]
	v_pk_add_f16 v36, v36, s5 op_sel_hi:[1,0]
	v_pk_add_f16 v37, v37, s5 op_sel_hi:[1,0]
	v_perm_b32 v142, v240, v152, s42
	v_perm_b32 v143, v240, v152, s43
	v_perm_b32 v144, v240, v153, s42
	v_perm_b32 v53, v240, v153, s43
	v_pk_add_f16 v50, v142, s5 op_sel_hi:[1,0]
	v_pk_add_f16 v51, v143, s5 op_sel_hi:[1,0]
	v_pk_add_f16 v52, v144, s5 op_sel_hi:[1,0]
	v_pk_add_f16 v53, v53, s5 op_sel_hi:[1,0]
	v_cvt_pk_f16_f32 v49, v48, v49
	v_cvt_pk_f16_f32 v48, v46, v47
	v_cvt_pk_f16_f32 v47, v44, v45
	v_cvt_pk_f16_f32 v46, v42, v43
	v_mfma_f32_32x32x16_f16 v[2:17], v[34:37], v[38:41], v[2:17]
	s_waitcnt vmcnt(5)
	v_lshlrev_b32_e32 v54, 8, v150
	v_mfma_f32_32x32x16_f16 v[18:33], v[50:53], v[38:41], v[18:33]
	v_lshrrev_b32_e32 v37, 16, v151
	v_lshrrev_b32_e32 v38, 8, v151
	v_perm_b32 v34, v54, v150, s4
	v_perm_b32 v37, v38, v37, s4
	v_perm_b32 v42, v240, v140, s42
	v_perm_b32 v43, v240, v140, s43
	v_perm_b32 v44, v240, v141, s42
	v_perm_b32 v45, v240, v141, s43
	v_or_b32_e32 v34, 0x64006400, v34
	v_perm_b32 v35, v240, v150, s43
	v_perm_b32 v36, v240, v151, s42
	v_or_b32_e32 v37, 0x64006400, v37
	v_pk_add_f16 v42, v42, s5 op_sel_hi:[1,0]
	v_pk_add_f16 v43, v43, s5 op_sel_hi:[1,0]
	v_pk_add_f16 v44, v44, s5 op_sel_hi:[1,0]
	v_pk_add_f16 v45, v45, s5 op_sel_hi:[1,0]
	v_pk_add_f16 v34, v34, s5 op_sel_hi:[1,0]
	v_pk_add_f16 v35, v35, s5 op_sel_hi:[1,0]
	v_pk_add_f16 v36, v36, s5 op_sel_hi:[1,0]
	v_pk_add_f16 v37, v37, s5 op_sel_hi:[1,0]
	v_mfma_f32_32x32x16_f16 v[2:17], v[42:45], v[46:49], v[2:17]
	global_load_dwordx2 v[142:143], v0, s[0:1] offset:2560
	global_load_dwordx2 v[140:141], v0, s[0:1] offset:3072
	global_load_dwordx2 v[64:65], v0, s[0:1] offset:3584
	v_mfma_f32_32x32x16_f16 v[18:33], v[34:37], v[46:49], v[18:33]
	s_nop 7
	v_add_f32_e32 v146, v157, v2
	v_add_f32_e32 v148, v157, v3
	v_cvt_pk_f16_f32 v0, v146, v148
	v_add_f32_e32 v150, v157, v4
	v_add_f32_e32 v152, v157, v5
	ds_write_b16 v158, v0
	v_add_f32_e32 v147, v157, v18
	v_cvt_f16_f32_e32 v2, v147
	v_add_f32_e32 v151, v157, v20
	v_add_f32_e32 v153, v157, v21
	ds_write_b16_d16_hi v158, v0 offset:144
	ds_write_b16 v158, v2 offset:4608
	v_cvt_pk_f16_f32 v0, v150, v151
	v_cvt_pk_f16_f32 v3, v152, v153
	v_add_f32_e32 v154, v157, v6
	v_add_f32_e32 v155, v157, v22
	v_add_f32_e32 v198, v157, v7
	v_add_f32_e32 v200, v157, v23
	ds_write_b16 v158, v0 offset:288
	ds_write_b16_d16_hi v158, v0 offset:4896
	ds_write_b16 v158, v3 offset:432
	ds_write_b16_d16_hi v158, v3 offset:5040
	v_cvt_pk_f16_f32 v0, v154, v155
	v_cvt_pk_f16_f32 v3, v198, v200
	v_add_f32_e32 v203, v157, v8
	v_add_f32_e32 v204, v157, v24
	v_add_f32_e32 v223, v157, v9
	v_add_f32_e32 v224, v157, v25
	ds_write_b16 v158, v0 offset:1152
	ds_write_b16_d16_hi v158, v0 offset:5760
	ds_write_b16 v158, v3 offset:1296
	ds_write_b16_d16_hi v158, v3 offset:5904
	v_cvt_pk_f16_f32 v0, v203, v204
	v_cvt_pk_f16_f32 v3, v223, v224
	v_add_f32_e32 v225, v157, v10
	v_add_f32_e32 v226, v157, v26
	v_add_f32_e32 v227, v157, v11
	v_add_f32_e32 v228, v157, v27
	ds_write_b16 v158, v0 offset:1440
	ds_write_b16_d16_hi v158, v0 offset:6048
	ds_write_b16 v158, v3 offset:1584
	ds_write_b16_d16_hi v158, v3 offset:6192
	v_cvt_pk_f16_f32 v0, v225, v226
	v_cvt_pk_f16_f32 v3, v227, v228
	v_add_f32_e32 v229, v157, v12
	v_add_f32_e32 v230, v157, v28
	v_add_f32_e32 v231, v157, v13
	v_add_f32_e32 v232, v157, v29
	ds_write_b16 v158, v0 offset:2304
	ds_write_b16_d16_hi v158, v0 offset:6912
	ds_write_b16 v158, v3 offset:2448
	ds_write_b16_d16_hi v158, v3 offset:7056
	v_cvt_pk_f16_f32 v0, v229, v230
	v_cvt_pk_f16_f32 v3, v231, v232
	v_add_f32_e32 v233, v157, v14
	v_add_f32_e32 v234, v157, v30
	v_add_f32_e32 v235, v157, v15
	v_add_f32_e32 v236, v157, v31
	ds_write_b16 v158, v0 offset:2592
	ds_write_b16_d16_hi v158, v0 offset:7200
	ds_write_b16 v158, v3 offset:2736
	ds_write_b16_d16_hi v158, v3 offset:7344
	v_cvt_pk_f16_f32 v0, v233, v234
	v_cvt_pk_f16_f32 v3, v235, v236
	v_add_f32_e32 v149, v157, v19
	v_add_f32_e32 v237, v157, v16
	v_add_f32_e32 v238, v157, v32
	v_add_f32_e32 v144, v157, v17
	v_add_f32_e32 v145, v157, v33
	v_cvt_pk_f16_f32 v18, v149, v237
	ds_write_b16 v158, v0 offset:3456
	ds_write_b16_d16_hi v158, v0 offset:8064
	ds_write_b16 v158, v3 offset:3600
	ds_write_b16_d16_hi v158, v3 offset:8208
	v_cvt_pk_f16_f32 v2, v238, v144
	v_cvt_f16_f32_e32 v4, v145
	ds_write_b16 v158, v18 offset:4752
	ds_write_b16_d16_hi v158, v18 offset:3744
	ds_write_b16 v158, v2 offset:8352
	ds_write_b16_d16_hi v158, v2 offset:3888
	ds_write_b16 v158, v4 offset:8496
	s_waitcnt lgkmcnt(0)
	s_barrier
	ds_read_b128 v[16:19], v159 offset:43520
	s_waitcnt lgkmcnt(0)
	v_mfma_f32_32x32x16_f16 v[32:47], v[16:19], v[126:129], 0
	ds_read_b128 v[2:5], v159 offset:34816
	v_mul_f32_e32 v0, v160, v160
	v_fmac_f32_e32 v0, v1, v1
	v_mul_f32_e32 v6, v162, v162
	v_add_f32_e32 v0, v0, v193
	v_add_f32_e32 v1, v161, v162
	v_fmac_f32_e32 v6, v161, v161
	s_waitcnt lgkmcnt(0)
	v_mfma_f32_32x32x16_f16 v[48:63], v[2:5], v[126:129], 0
	ds_read_b128 v[126:129], v159 offset:34848
	v_add_f32_e32 v1, v1, v196
	v_add_f32_e32 v0, v6, v0
	v_add_f32_e32 v6, v163, v164
	v_add_f32_e32 v1, v6, v1
	v_mul_f32_e32 v6, v164, v164
	v_fmac_f32_e32 v6, v163, v163
	v_add_f32_e32 v0, v6, v0
	v_add_f32_e32 v6, v165, v166
	v_add_f32_e32 v1, v6, v1
	v_mul_f32_e32 v6, v166, v166
	v_fmac_f32_e32 v6, v165, v165
	v_add_f32_e32 v20, v6, v0
	v_add_f32_e32 v0, v167, v168
	v_add_f32_e32 v21, v0, v1
	s_waitcnt lgkmcnt(0)
	v_mfma_f32_32x32x16_f16 v[48:63], v[126:129], v[118:121], v[48:63]
	v_mul_f32_e32 v22, v168, v168
	v_fmac_f32_e32 v22, v167, v167
	v_add_f32_e32 v160, v22, v20
	v_add_f32_e32 v20, v169, v170
	v_mul_f32_e32 v162, v170, v170
	v_add_f32_e32 v161, v20, v21
	v_fmac_f32_e32 v162, v169, v169
	v_mfma_f32_32x32x16_f16 v[0:15], v[2:5], v[122:125], 0
	v_mfma_f32_32x32x16_f16 v[0:15], v[126:129], v[114:117], v[0:15]
	v_mfma_f32_32x32x16_f16 v[16:31], v[16:19], v[122:125], 0
	v_add_f32_e32 v123, v171, v172
	v_add_f32_e32 v122, v162, v160
	v_add_f32_e32 v160, v123, v161
	v_mul_f32_e32 v123, v172, v172
	v_fmac_f32_e32 v123, v171, v171
	v_add_f32_e32 v161, v123, v122
	ds_read_b128 v[122:125], v159 offset:43552
	v_add_f32_e32 v162, v173, v174
	v_add_f32_e32 v160, v162, v160
	v_mul_f32_e32 v162, v174, v174
	v_fmac_f32_e32 v162, v173, v173
	s_waitcnt lgkmcnt(0)
	v_mfma_f32_32x32x16_f16 v[32:47], v[122:125], v[118:121], v[32:47]
	v_mul_f32_e32 v118, v176, v176
	v_add_f32_e32 v161, v162, v161
	v_add_f32_e32 v162, v175, v176
	v_fmac_f32_e32 v118, v175, v175
	v_mul_f32_e32 v120, v178, v178
	v_add_f32_e32 v160, v162, v160
	v_add_f32_e32 v118, v118, v161
	v_add_f32_e32 v119, v177, v178
	v_fmac_f32_e32 v120, v177, v177
	v_add_f32_e32 v119, v119, v160
	v_add_f32_e32 v118, v120, v118
	v_add_f32_e32 v120, v179, v180
	v_add_f32_e32 v126, v120, v119
	v_mul_f32_e32 v119, v180, v180
	v_mfma_f32_32x32x16_f16 v[16:31], v[122:125], v[114:117], v[16:31]
	v_add_f32_e32 v114, v181, v183
	v_fmac_f32_e32 v119, v179, v179
	v_add_f32_e32 v122, v114, v126
	v_mul_f32_e32 v114, v183, v183
	v_add_f32_e32 v127, v119, v118
	v_fmac_f32_e32 v114, v181, v181
	ds_read_b128 v[118:121], v159 offset:34880
	v_add_f32_e32 v123, v114, v127
	ds_read_b128 v[114:117], v159 offset:43584
	v_add_f32_e32 v124, v182, v184
	v_add_f32_e32 v122, v124, v122
	v_mul_f32_e32 v124, v184, v184
	v_fmac_f32_e32 v124, v182, v182
	s_waitcnt lgkmcnt(1)
	v_mfma_f32_32x32x16_f16 v[48:63], v[118:121], v[110:113], v[48:63]
	v_add_f32_e32 v123, v124, v123
	v_add_f32_e32 v124, v185, v186
	v_add_f32_e32 v124, 0, v124
	v_add_f32_e32 v122, 0, v122
	s_waitcnt lgkmcnt(0)
	v_mfma_f32_32x32x16_f16 v[32:47], v[114:117], v[110:113], v[32:47]
	v_mul_f32_e32 v110, v186, v186
	v_mul_f32_e32 v112, v188, v188
	v_fmac_f32_e32 v110, v185, v185
	v_add_f32_e32 v111, v187, v188
	v_fmac_f32_e32 v112, v187, v187
	v_add_f32_e32 v111, v111, v124
	v_add_f32_e32 v110, v110, v112
	v_add_f32_e32 v112, v189, v190
	v_mfma_f32_32x32x16_f16 v[0:15], v[118:121], v[106:109], v[0:15]
	v_add_f32_e32 v118, v112, v111
	v_mul_f32_e32 v111, v190, v190
	v_fmac_f32_e32 v111, v189, v189
	v_add_f32_e32 v119, v111, v110
	v_add_f32_e32 v120, v191, v192
	ds_read_b128 v[110:113], v159 offset:34912
	v_mfma_f32_32x32x16_f16 v[16:31], v[114:117], v[106:109], v[16:31]
	v_mul_f32_e32 v107, v192, v192
	v_fmac_f32_e32 v107, v191, v191
	v_add_f32_e32 v106, v120, v118
	v_add_f32_e32 v114, v107, v119
	v_add_f32_e32 v107, v194, v195
	v_add_f32_e32 v115, v107, v106
	ds_read_b128 v[106:109], v159 offset:43616
	v_mul_f32_e32 v116, v195, v195
	v_fmac_f32_e32 v116, v194, v194
	v_add_f32_e32 v114, v116, v114
	v_add_f32_e32 v116, v197, v199
	v_add_f32_e32 v115, v116, v115
	v_mul_f32_e32 v116, v199, v199
	s_waitcnt lgkmcnt(1)
	v_mfma_f32_32x32x16_f16 v[48:63], v[110:113], v[102:105], v[48:63]
	v_fmac_f32_e32 v116, v197, v197
	s_waitcnt lgkmcnt(0)
	v_mfma_f32_32x32x16_f16 v[32:47], v[106:109], v[102:105], v[32:47]
	v_mul_f32_e32 v104, v202, v202
	v_add_f32_e32 v102, v116, v114
	v_add_f32_e32 v103, v201, v202
	v_fmac_f32_e32 v104, v201, v201
	v_add_f32_e32 v103, v103, v115
	v_add_f32_e32 v102, v104, v102
	v_add_f32_e32 v104, v205, v206
	v_add_f32_e32 v103, v104, v103
	v_mul_f32_e32 v104, v206, v206
	v_mfma_f32_32x32x16_f16 v[0:15], v[110:113], v[98:101], v[0:15]
	v_fmac_f32_e32 v104, v205, v205
	v_add_f32_e32 v110, v104, v102
	v_add_f32_e32 v102, v207, v209
	v_add_f32_e32 v111, v102, v103
	ds_read_b128 v[102:105], v159 offset:34944
	v_mfma_f32_32x32x16_f16 v[16:31], v[106:109], v[98:101], v[16:31]
	v_mul_f32_e32 v98, v209, v209
	v_fmac_f32_e32 v98, v207, v207
	v_add_f32_e32 v106, v98, v110
	v_add_f32_e32 v98, v208, v210
	v_add_f32_e32 v107, v98, v111
	ds_read_b128 v[98:101], v159 offset:43648
	v_mul_f32_e32 v108, v210, v210
	v_fmac_f32_e32 v108, v208, v208
	v_add_f32_e32 v106, v108, v106
	v_add_f32_e32 v108, v211, v212
	s_waitcnt lgkmcnt(1)
	v_mfma_f32_32x32x16_f16 v[48:63], v[102:105], v[94:97], v[48:63]
	v_add_f32_e32 v107, v108, v107
	v_mul_f32_e32 v108, v212, v212
	v_fmac_f32_e32 v108, v211, v211
	v_add_f32_e32 v106, v108, v106
	s_waitcnt lgkmcnt(0)
	v_mfma_f32_32x32x16_f16 v[32:47], v[98:101], v[94:97], v[32:47]
	v_add_f32_e32 v94, v213, v214
	v_add_f32_e32 v94, v94, v107
	v_mul_f32_e32 v95, v214, v214
	v_add_f32_e32 v96, v215, v216
	v_fmac_f32_e32 v95, v213, v213
	v_add_f32_e32 v94, v96, v94
	v_mul_f32_e32 v96, v216, v216
	v_add_f32_e32 v95, v95, v106
	v_fmac_f32_e32 v96, v215, v215
	v_mfma_f32_32x32x16_f16 v[0:15], v[102:105], v[86:89], v[0:15]
	v_add_f32_e32 v102, v96, v95
	v_add_f32_e32 v95, v217, v218
	v_add_f32_e32 v103, v95, v94
	ds_read_b128 v[94:97], v159 offset:34976
	v_mul_f32_e32 v104, v218, v218
	v_fmac_f32_e32 v104, v217, v217
	v_mfma_f32_32x32x16_f16 v[16:31], v[98:101], v[86:89], v[16:31]
	v_add_f32_e32 v86, v219, v221
	v_add_f32_e32 v99, v86, v103
	ds_read_b128 v[86:89], v159 offset:43680
	v_mul_f32_e32 v100, v221, v221
	v_add_f32_e32 v98, v104, v102
	v_fmac_f32_e32 v100, v219, v219
	v_add_f32_e32 v98, v100, v98
	s_waitcnt lgkmcnt(1)
	v_mfma_f32_32x32x16_f16 v[48:63], v[94:97], v[90:93], v[48:63]
	v_add_f32_e32 v100, v220, v222
	v_add_f32_e32 v99, v100, v99
	v_mul_f32_e32 v100, v222, v222
	v_fmac_f32_e32 v100, v220, v220
	v_add_f32_e32 v98, v100, v98
	v_add_f32_e32 v98, v123, v98
	v_add_f32_e32 v99, v122, v99
	s_waitcnt lgkmcnt(0)
	v_mfma_f32_32x32x16_f16 v[32:47], v[86:89], v[90:93], v[32:47]
	v_add_f32_e32 v90, v146, v147
	v_add_f32_e32 v90, 0, v90
	v_add_f32_e32 v92, v148, v149
	v_mul_f32_e32 v91, v147, v147
	v_add_f32_e32 v90, v92, v90
	v_mul_f32_e32 v92, v149, v149
	v_fmac_f32_e32 v91, v146, v146
	v_fmac_f32_e32 v92, v148, v148
	v_mfma_f32_32x32x16_f16 v[0:15], v[94:97], v[78:81], v[0:15]
	v_add_f32_e32 v94, v91, v92
	v_add_f32_e32 v91, v150, v151
	v_add_f32_e32 v95, v91, v90
	ds_read_b128 v[90:93], v159 offset:35008
	v_mul_f32_e32 v96, v151, v151
	v_fmac_f32_e32 v96, v150, v150
	v_mfma_f32_32x32x16_f16 v[16:31], v[86:89], v[78:81], v[16:31]
	v_add_f32_e32 v78, v152, v153
	v_add_f32_e32 v87, v78, v95
	ds_read_b128 v[78:81], v159 offset:43712
	v_mul_f32_e32 v88, v153, v153
	v_add_f32_e32 v86, v96, v94
	v_fmac_f32_e32 v88, v152, v152
	v_add_f32_e32 v86, v88, v86
	v_add_f32_e32 v88, v154, v155
	v_add_f32_e32 v87, v88, v87
	v_mul_f32_e32 v88, v155, v155
	v_fmac_f32_e32 v88, v154, v154
	v_add_f32_e32 v86, v88, v86
	v_add_f32_e32 v88, v198, v200
	s_waitcnt lgkmcnt(1)
	v_mfma_f32_32x32x16_f16 v[48:63], v[90:93], v[82:85], v[48:63]
	s_waitcnt lgkmcnt(0)
	v_mfma_f32_32x32x16_f16 v[32:47], v[78:81], v[82:85], v[32:47]
	v_add_f32_e32 v82, v88, v87
	v_mul_f32_e32 v83, v200, v200
	v_add_f32_e32 v84, v203, v204
	v_fmac_f32_e32 v83, v198, v198
	v_add_f32_e32 v82, v84, v82
	v_mul_f32_e32 v84, v204, v204
	v_add_f32_e32 v83, v83, v86
	v_fmac_f32_e32 v84, v203, v203
	v_add_f32_e32 v86, v84, v83
	v_add_f32_e32 v83, v223, v224
	v_mfma_f32_32x32x16_f16 v[0:15], v[90:93], v[70:73], v[0:15]
	v_add_f32_e32 v87, v83, v82
	v_mul_f32_e32 v88, v224, v224
	v_fmac_f32_e32 v88, v223, v223
	ds_read_b128 v[82:85], v159 offset:35040
	v_mfma_f32_32x32x16_f16 v[16:31], v[78:81], v[70:73], v[16:31]
	v_add_f32_e32 v71, v225, v226
	v_add_f32_e32 v78, v71, v87
	v_mul_f32_e32 v71, v226, v226
	v_add_f32_e32 v70, v88, v86
	v_fmac_f32_e32 v71, v225, v225
	v_add_f32_e32 v79, v71, v70
	ds_read_b128 v[70:73], v159 offset:43744
	s_waitcnt lgkmcnt(1)
	v_mfma_f32_32x32x16_f16 v[48:63], v[82:85], v[74:77], v[48:63]
	v_add_f32_e32 v80, v227, v228
	v_add_f32_e32 v78, v80, v78
	v_mul_f32_e32 v80, v228, v228
	v_fmac_f32_e32 v80, v227, v227
	v_add_f32_e32 v79, v80, v79
	v_add_f32_e32 v80, v229, v230
	v_add_f32_e32 v78, v80, v78
	v_mfma_f32_32x32x16_f16 v[0:15], v[82:85], v[66:69], v[0:15]
	s_nop 3
	v_cvt_pk_f16_f32 v55, v54, v55
	v_cvt_pk_f16_f32 v54, v52, v53
	v_cvt_pk_f16_f32 v53, v50, v51
	v_cvt_pk_f16_f32 v52, v48, v49
	s_waitcnt vmcnt(3)
	s_waitcnt lgkmcnt(0)
	v_mfma_f32_32x32x16_f16 v[16:31], v[70:73], v[66:69], v[16:31]
	v_lshrrev_b32_e32 v69, 16, v139
	v_mfma_f32_32x32x16_f16 v[32:47], v[70:73], v[74:77], v[32:47]
	v_lshrrev_b32_e32 v70, 8, v139
	v_perm_b32 v69, v70, v69, s4
	v_perm_b32 v66, v240, v138, s42
	v_perm_b32 v67, v240, v138, s43
	v_perm_b32 v68, v240, v139, s42
	v_or_b32_e32 v69, 0x64006400, v69
	v_pk_add_f16 v66, v66, s5 op_sel_hi:[1,0]
	v_pk_add_f16 v67, v67, s5 op_sel_hi:[1,0]
	v_pk_add_f16 v68, v68, s5 op_sel_hi:[1,0]
	v_pk_add_f16 v69, v69, s5 op_sel_hi:[1,0]
	s_nop 1
	v_mfma_f32_32x32x16_f16 v[0:15], v[66:69], v[52:55], v[0:15]
	v_perm_b32 v48, v240, v136, s42
	v_perm_b32 v49, v240, v136, s43
	v_perm_b32 v50, v240, v137, s42
	v_perm_b32 v51, v240, v137, s43
	v_pk_add_f16 v48, v48, s5 op_sel_hi:[1,0]
	v_pk_add_f16 v49, v49, s5 op_sel_hi:[1,0]
	v_pk_add_f16 v50, v50, s5 op_sel_hi:[1,0]
	v_pk_add_f16 v51, v51, s5 op_sel_hi:[1,0]
	v_cvt_pk_f16_f32 v39, v38, v39
	v_cvt_pk_f16_f32 v38, v36, v37
	v_mfma_f32_32x32x16_f16 v[16:31], v[48:51], v[52:55], v[16:31]
	v_perm_b32 v48, v240, v134, s42
	v_perm_b32 v49, v240, v134, s43
	v_perm_b32 v50, v240, v135, s42
	v_perm_b32 v51, v240, v135, s43
	v_pk_add_f16 v48, v48, s5 op_sel_hi:[1,0]
	v_pk_add_f16 v49, v49, s5 op_sel_hi:[1,0]
	v_pk_add_f16 v50, v50, s5 op_sel_hi:[1,0]
	v_pk_add_f16 v51, v51, s5 op_sel_hi:[1,0]
	v_cvt_pk_f16_f32 v55, v62, v63
	v_cvt_pk_f16_f32 v54, v60, v61
	v_cvt_pk_f16_f32 v53, v58, v59
	v_cvt_pk_f16_f32 v52, v56, v57
	s_waitcnt vmcnt(2)
	v_cvt_pk_f16_f32 v37, v34, v35
	v_mfma_f32_32x32x16_f16 v[0:15], v[48:51], v[52:55], v[0:15]
	v_perm_b32 v48, v240, v142, s42
	v_perm_b32 v49, v240, v142, s43
	v_perm_b32 v50, v240, v143, s42
	v_perm_b32 v51, v240, v143, s43
	v_pk_add_f16 v48, v48, s5 op_sel_hi:[1,0]
	v_pk_add_f16 v49, v49, s5 op_sel_hi:[1,0]
	v_pk_add_f16 v50, v50, s5 op_sel_hi:[1,0]
	v_pk_add_f16 v51, v51, s5 op_sel_hi:[1,0]
	v_cvt_pk_f16_f32 v36, v32, v33
	s_waitcnt vmcnt(1)
	v_mfma_f32_32x32x16_f16 v[16:31], v[48:51], v[52:55], v[16:31]
	v_lshrrev_b32_e32 v51, 16, v133
	v_lshrrev_b32_e32 v52, 8, v133
	v_perm_b32 v51, v52, v51, s4
	v_perm_b32 v48, v240, v132, s42
	v_perm_b32 v49, v240, v132, s43
	v_perm_b32 v50, v240, v133, s42
	v_or_b32_e32 v51, 0x64006400, v51
	v_pk_add_f16 v48, v48, s5 op_sel_hi:[1,0]
	v_pk_add_f16 v49, v49, s5 op_sel_hi:[1,0]
	v_pk_add_f16 v50, v50, s5 op_sel_hi:[1,0]
	v_pk_add_f16 v51, v51, s5 op_sel_hi:[1,0]
	s_nop 1
	v_mfma_f32_32x32x16_f16 v[0:15], v[48:51], v[36:39], v[0:15]
	v_perm_b32 v32, v240, v140, s42
	v_perm_b32 v33, v240, v140, s43
	v_perm_b32 v34, v240, v141, s42
	v_perm_b32 v35, v240, v141, s43
	v_pk_add_f16 v32, v32, s5 op_sel_hi:[1,0]
	v_pk_add_f16 v33, v33, s5 op_sel_hi:[1,0]
	v_pk_add_f16 v34, v34, s5 op_sel_hi:[1,0]
	v_pk_add_f16 v35, v35, s5 op_sel_hi:[1,0]
	v_mul_f32_e32 v74, v230, v230
	v_fmac_f32_e32 v74, v229, v229
	v_mfma_f32_32x32x16_f16 v[16:31], v[32:35], v[36:39], v[16:31]
	v_perm_b32 v32, v240, v130, s42
	v_perm_b32 v33, v240, v130, s43
	v_perm_b32 v34, v240, v131, s42
	v_perm_b32 v35, v240, v131, s43
	v_pk_add_f16 v32, v32, s5 op_sel_hi:[1,0]
	v_pk_add_f16 v33, v33, s5 op_sel_hi:[1,0]
	v_pk_add_f16 v34, v34, s5 op_sel_hi:[1,0]
	v_pk_add_f16 v35, v35, s5 op_sel_hi:[1,0]
	v_cvt_pk_f16_f32 v39, v46, v47
	v_cvt_pk_f16_f32 v38, v44, v45
	v_cvt_pk_f16_f32 v37, v42, v43
	v_cvt_pk_f16_f32 v36, v40, v41
	s_waitcnt vmcnt(0)
	v_mul_f32_e32 v76, v232, v232
	v_mfma_f32_32x32x16_f16 v[0:15], v[32:35], v[36:39], v[0:15]
	v_perm_b32 v32, v240, v64, s42
	v_perm_b32 v33, v240, v64, s43
	v_perm_b32 v34, v240, v65, s42
	v_perm_b32 v35, v240, v65, s43
	v_pk_add_f16 v32, v32, s5 op_sel_hi:[1,0]
	v_pk_add_f16 v33, v33, s5 op_sel_hi:[1,0]
	v_pk_add_f16 v34, v34, s5 op_sel_hi:[1,0]
	v_pk_add_f16 v35, v35, s5 op_sel_hi:[1,0]
	s_nop 3
	v_add_f32_e32 v0, v157, v0
	v_add_f32_e32 v74, v74, v79
	v_mfma_f32_32x32x16_f16 v[16:31], v[32:35], v[36:39], v[16:31]
	v_cvt_f16_f32_e32 v33, v0
	v_add_f32_e32 v75, v231, v232
	v_fmac_f32_e32 v76, v231, v231
	v_add_f32_e32 v75, v75, v78
	ds_write_b16 v158, v33 offset:18432
	v_add_f32_e32 v74, v76, v74
	v_add_f32_e32 v76, v233, v234
	s_nop 4
	v_add_f32_e32 v16, v157, v16
	v_add_f32_e32 v32, v0, v16
	v_cvt_f16_f32_e32 v34, v16
	v_mul_f32_e32 v16, v16, v16
	v_fmac_f32_e32 v16, v0, v0
	v_add_f32_e32 v0, v157, v1
	v_add_f32_e32 v1, v157, v17
	v_add_f32_e32 v32, 0, v32
	v_add_f32_e32 v17, v0, v1
	v_add_f32_e32 v17, v17, v32
	v_mul_f32_e32 v32, v1, v1
	v_cvt_f16_f32_e32 v1, v1
	v_fmac_f32_e32 v32, v0, v0
	v_cvt_f16_f32_e32 v33, v0
	v_add_f32_e32 v0, v16, v32
	ds_write_b16 v158, v1 offset:23184
	v_add_f32_e32 v1, v157, v2
	v_add_f32_e32 v2, v157, v18
	v_add_f32_e32 v16, v1, v2
	v_add_f32_e32 v16, v16, v17
	v_mul_f32_e32 v17, v2, v2
	v_cvt_f16_f32_e32 v2, v2
	v_cvt_f16_f32_e32 v18, v1
	v_fmac_f32_e32 v17, v1, v1
	v_add_f32_e32 v1, v157, v3
	ds_write_b16 v158, v2 offset:23328
	v_add_f32_e32 v2, v157, v19
	v_add_f32_e32 v3, v1, v2
	v_add_f32_e32 v3, v3, v16
	v_mul_f32_e32 v16, v2, v2
	v_cvt_f16_f32_e32 v2, v2
	v_add_f32_e32 v0, v17, v0
	v_cvt_f16_f32_e32 v17, v1
	v_fmac_f32_e32 v16, v1, v1
	ds_write_b16 v158, v2 offset:23472
	v_add_f32_e32 v1, v157, v4
	v_add_f32_e32 v2, v157, v20
	v_add_f32_e32 v4, v1, v2
	v_add_f32_e32 v3, v4, v3
	v_mul_f32_e32 v4, v2, v2
	v_cvt_f16_f32_e32 v2, v2
	v_add_f32_e32 v0, v16, v0
	v_cvt_f16_f32_e32 v16, v1
	v_fmac_f32_e32 v4, v1, v1
	ds_write_b16 v158, v2 offset:24192
	v_add_f32_e32 v1, v157, v5
	v_add_f32_e32 v2, v157, v21
	v_add_f32_e32 v0, v4, v0
	v_add_f32_e32 v4, v1, v2
	v_add_f32_e32 v3, v4, v3
	v_mul_f32_e32 v4, v2, v2
	v_cvt_f16_f32_e32 v2, v2
	v_cvt_f16_f32_e32 v5, v1
	v_fmac_f32_e32 v4, v1, v1
	v_add_f32_e32 v1, v157, v6
	ds_write_b16 v158, v2 offset:24336
	v_add_f32_e32 v2, v157, v22
	v_add_f32_e32 v0, v4, v0
	v_add_f32_e32 v4, v1, v2
	v_add_f32_e32 v3, v4, v3
	v_mul_f32_e32 v4, v2, v2
	v_cvt_f16_f32_e32 v2, v2
	ds_write_b16 v158, v5 offset:19728
	v_cvt_f16_f32_e32 v5, v1
	v_fmac_f32_e32 v4, v1, v1
	ds_write_b16 v158, v2 offset:24480
	v_add_f32_e32 v1, v157, v7
	v_add_f32_e32 v2, v157, v23
	v_add_f32_e32 v0, v4, v0
	v_add_f32_e32 v4, v1, v2
	v_add_f32_e32 v3, v4, v3
	v_mul_f32_e32 v4, v2, v2
	v_cvt_f16_f32_e32 v2, v2
	ds_write_b16 v158, v5 offset:19872
	v_cvt_f16_f32_e32 v5, v1
	v_fmac_f32_e32 v4, v1, v1
	ds_write_b16 v158, v2 offset:24624
	v_add_f32_e32 v1, v157, v8
	v_add_f32_e32 v2, v157, v24
	v_add_f32_e32 v0, v4, v0
	v_add_f32_e32 v4, v1, v2
	v_add_f32_e32 v3, v4, v3
	v_mul_f32_e32 v4, v2, v2
	v_cvt_f16_f32_e32 v2, v2
	ds_write_b16 v158, v5 offset:20016
	v_cvt_f16_f32_e32 v5, v1
	v_fmac_f32_e32 v4, v1, v1
	ds_write_b16 v158, v2 offset:25344
	v_add_f32_e32 v1, v157, v9
	v_add_f32_e32 v2, v157, v25
	v_add_f32_e32 v0, v4, v0
	v_add_f32_e32 v4, v1, v2
	v_add_f32_e32 v3, v4, v3
	v_mul_f32_e32 v4, v2, v2
	v_cvt_f16_f32_e32 v2, v2
	ds_write_b16 v158, v5 offset:20736
	v_cvt_f16_f32_e32 v5, v1
	v_fmac_f32_e32 v4, v1, v1
	ds_write_b16 v158, v2 offset:25488
	v_add_f32_e32 v1, v157, v10
	v_add_f32_e32 v2, v157, v26
	v_add_f32_e32 v0, v4, v0
	v_add_f32_e32 v4, v1, v2
	v_add_f32_e32 v3, v4, v3
	v_mul_f32_e32 v4, v2, v2
	v_cvt_f16_f32_e32 v2, v2
	ds_write_b16 v158, v5 offset:20880
	v_cvt_f16_f32_e32 v5, v1
	v_fmac_f32_e32 v4, v1, v1
	ds_write_b16 v158, v2 offset:25632
	v_add_f32_e32 v1, v157, v11
	v_add_f32_e32 v2, v157, v27
	v_add_f32_e32 v0, v4, v0
	v_add_f32_e32 v4, v1, v2
	v_add_f32_e32 v3, v4, v3
	v_mul_f32_e32 v4, v2, v2
	v_cvt_f16_f32_e32 v2, v2
	ds_write_b16 v158, v5 offset:21024
	v_cvt_f16_f32_e32 v5, v1
	v_fmac_f32_e32 v4, v1, v1
	ds_write_b16 v158, v2 offset:25776
	v_add_f32_e32 v1, v157, v12
	v_add_f32_e32 v2, v157, v28
	v_add_f32_e32 v0, v4, v0
	v_add_f32_e32 v4, v1, v2
	v_add_f32_e32 v3, v4, v3
	v_mul_f32_e32 v4, v2, v2
	v_cvt_f16_f32_e32 v2, v2
	ds_write_b16 v158, v5 offset:21168
	v_cvt_f16_f32_e32 v5, v1
	v_fmac_f32_e32 v4, v1, v1
	ds_write_b16 v158, v2 offset:26496
	v_add_f32_e32 v1, v157, v13
	v_add_f32_e32 v2, v157, v29
	v_add_f32_e32 v0, v4, v0
	v_add_f32_e32 v4, v1, v2
	v_add_f32_e32 v3, v4, v3
	v_mul_f32_e32 v4, v2, v2
	v_cvt_f16_f32_e32 v2, v2
	ds_write_b16 v158, v5 offset:21888
	v_cvt_f16_f32_e32 v5, v1
	v_fmac_f32_e32 v4, v1, v1
	ds_write_b16 v158, v2 offset:26640
	v_add_f32_e32 v1, v157, v14
	v_add_f32_e32 v2, v157, v30
	v_add_f32_e32 v0, v4, v0
	v_add_f32_e32 v4, v1, v2
	v_add_f32_e32 v3, v4, v3
	v_cvt_f16_f32_e32 v4, v1
	v_add_f32_e32 v75, v76, v75
	v_mul_f32_e32 v76, v234, v234
	ds_write_b16 v158, v5 offset:22032
	v_mul_f32_e32 v5, v2, v2
	v_fmac_f32_e32 v76, v233, v233
	v_mul_f32_e32 v67, v236, v236
	v_fmac_f32_e32 v5, v1, v1
	v_add_f32_e32 v74, v76, v74
	v_fmac_f32_e32 v67, v235, v235
	v_mul_f32_e32 v57, v238, v238
	v_add_f32_e32 v0, v5, v0
	v_cvt_f16_f32_e32 v5, v2
	v_add_f32_e32 v1, v157, v15
	v_add_f32_e32 v2, v157, v31
	v_add_f32_e32 v76, v235, v236
	v_add_f32_e32 v67, v67, v74
	v_fmac_f32_e32 v57, v237, v237
	v_mul_f32_e32 v50, v145, v145
	ds_write_b16 v158, v4 offset:22176
	v_add_f32_e32 v4, v1, v2
	v_add_f32_e32 v66, v76, v75
	v_add_f32_e32 v56, v237, v238
	v_add_f32_e32 v48, v57, v67
	v_fmac_f32_e32 v50, v144, v144
	v_add_f32_e32 v3, v4, v3
	v_mul_f32_e32 v4, v2, v2
	v_add_f32_e32 v56, v56, v66
	v_add_f32_e32 v49, v144, v145
	v_add_f32_e32 v40, v50, v48
	v_fmac_f32_e32 v4, v1, v1
	v_add_f32_e32 v49, v49, v56
	v_add_f32_e32 v40, v98, v40
	v_add_f32_e32 v4, v4, v0
	v_add_f32_e32 v41, v99, v49
	v_cvt_pk_f16_f32 v6, v1, v2
	v_add_f32_e32 v1, v40, v4
	v_lshlrev_b32_e32 v4, 2, v156
	v_add_f32_e32 v0, v41, v3
	v_xor_b32_e32 v3, 0x80, v4
	s_nop 0
	ds_bpermute_b32 v2, v3, v0
	ds_bpermute_b32 v3, v3, v1
	ds_write_b16 v158, v34 offset:23040
	ds_write_b16 v158, v33 offset:18576
	ds_write_b16 v158, v18 offset:18720
	ds_write_b16 v158, v17 offset:18864
	ds_write_b16 v158, v16 offset:19584
	ds_write_b16 v158, v5 offset:26784
	ds_write_b16 v158, v6 offset:22320
	ds_write_b16_d16_hi v158, v6 offset:26928
	s_and_saveexec_b64 s[0:1], vcc
	s_cbranch_execz .LBB2_26
	s_lshl_b32 s2, s10, 5
	v_lshl_add_u32 v4, s2, 2, v4
	v_or_b32_e32 v5, 0x1e400, v4
	s_waitcnt lgkmcnt(9)
	v_add_f32_e32 v0, v0, v2
	v_add_u32_e32 v4, 0x1e500, v4
	s_waitcnt lgkmcnt(8)
	v_add_f32_e32 v1, v1, v3
	ds_add_f32 v5, v0
	ds_add_f32 v4, v1

	.amdhsa_kernel _Z7k_layerILi1EEvPKDF16_S1_PKfS3_S3_S3_S3_S3_S1_S1_S1_S1_S3_S3_PKhS5_PDF16_S6_PfS7_
		.amdhsa_group_segment_fixed_size 126720
		.amdhsa_private_segment_fixed_size 0
		.amdhsa_kernarg_size 160
		.amdhsa_user_sgpr_count 2
		.amdhsa_user_sgpr_dispatch_ptr 0
		.amdhsa_user_sgpr_queue_ptr 0
		.amdhsa_user_sgpr_kernarg_segment_ptr 1
		.amdhsa_user_sgpr_dispatch_id 0
		.amdhsa_user_sgpr_kernarg_preload_length 0
		.amdhsa_user_sgpr_kernarg_preload_offset 0
		.amdhsa_user_sgpr_private_segment_size 0
		.amdhsa_uses_dynamic_stack 0
		.amdhsa_enable_private_segment 0
		.amdhsa_system_sgpr_workgroup_id_x 1
		.amdhsa_system_sgpr_workgroup_id_y 0
		.amdhsa_system_sgpr_workgroup_id_z 0
		.amdhsa_system_sgpr_workgroup_info 0
		.amdhsa_system_vgpr_workitem_id 0
		.amdhsa_next_free_vgpr 256
		.amdhsa_next_free_sgpr 96
		.amdhsa_accum_offset 256
		.amdhsa_reserve_vcc 1
		.amdhsa_float_round_mode_32 0
		.amdhsa_float_round_mode_16_64 0
		.amdhsa_float_denorm_mode_32 3
		.amdhsa_float_denorm_mode_16_64 3
		.amdhsa_dx10_clamp 1
		.amdhsa_ieee_mode 1
		.amdhsa_fp16_overflow 0
		.amdhsa_tg_split 0
		.amdhsa_exception_fp_ieee_invalid_op 0
		.amdhsa_exception_fp_denorm_src 0
		.amdhsa_exception_fp_ieee_div_zero 0
		.amdhsa_exception_fp_ieee_overflow 0
		.amdhsa_exception_fp_ieee_underflow 0
		.amdhsa_exception_fp_ieee_inexact 0
		.amdhsa_exception_int_div_zero 0
	.end_amdhsa_kernel

.LBB3_24:
	s_or_b64 exec, exec, s[2:3]
	v_and_b32_e32 v1, 31, v0
	v_lshlrev_b32_e32 v2, 2, v1
	v_lshl_or_b32 v2, s13, 7, v2
	v_or_b32_e32 v2, 0x1ee00, v2
	v_lshrrev_b32_e32 v158, 5, v156
	s_waitcnt lgkmcnt(0)
	s_barrier
	s_barrier
	ds_read_b32 v157, v2
	v_mul_u32_u24_e32 v2, 0x88, v1
	s_mul_i32 s0, s16, 0x4400
	v_lshlrev_b32_e32 v2, 1, v2
	v_lshlrev_b32_e32 v3, 4, v158
	v_mov_b32_e32 v138, v0
	v_add3_u32 v159, s0, v2, v3
	ds_read_b128 v[2:5], v159
	ds_read_b128 v[18:21], v159 offset:8704
	ds_read_b128 v[130:133], v159 offset:32
	s_waitcnt vmcnt(10) lgkmcnt(2)
	v_mfma_f32_32x32x16_f16 v[50:65], v[2:5], v[126:129], 0
	s_mov_b32 s2, 0xc060c00
	s_mov_b32 s3, 0xe400
	s_mulk_i32 s16, 0x2400
	s_lshl_b32 s0, s13, 6
	s_or_b32 s0, s16, s0
	s_add_i32 s0, s0, 0x11000
	v_lshl_or_b32 v1, v1, 1, s0
	s_waitcnt lgkmcnt(1)
	v_mfma_f32_32x32x16_f16 v[34:49], v[18:21], v[126:129], 0
	s_or_b32 s0, s10, 2
	s_ashr_i32 s1, s0, 31
	s_lshl_b64 s[0:1], s[0:1], 12
	s_add_u32 s0, s8, s0
	s_addc_u32 s1, s9, s1
	v_cmp_gt_u32_e32 vcc, 32, v156
	v_mfma_f32_32x32x16_f16 v[2:17], v[2:5], v[122:125], 0
	v_mfma_f32_32x32x16_f16 v[18:33], v[18:21], v[122:125], 0
	ds_read_b128 v[134:137], v159 offset:8736
	ds_read_b128 v[160:163], v159 offset:64
	s_waitcnt vmcnt(8) lgkmcnt(2)
	v_mfma_f32_32x32x16_f16 v[50:65], v[130:133], v[118:121], v[50:65]
	s_waitcnt lgkmcnt(1)
	v_mfma_f32_32x32x16_f16 v[34:49], v[134:137], v[118:121], v[34:49]
	v_mfma_f32_32x32x16_f16 v[2:17], v[130:133], v[114:117], v[2:17]
	v_mfma_f32_32x32x16_f16 v[18:33], v[134:137], v[114:117], v[18:33]
	ds_read_b128 v[130:133], v159 offset:8768
	ds_read_b128 v[134:137], v159 offset:96
	s_waitcnt vmcnt(6) lgkmcnt(2)
	v_mfma_f32_32x32x16_f16 v[50:65], v[160:163], v[110:113], v[50:65]
	s_waitcnt lgkmcnt(1)
	v_mfma_f32_32x32x16_f16 v[34:49], v[130:133], v[110:113], v[34:49]
	v_mfma_f32_32x32x16_f16 v[2:17], v[160:163], v[106:109], v[2:17]
	v_mfma_f32_32x32x16_f16 v[18:33], v[130:133], v[106:109], v[18:33]
	ds_read_b128 v[130:133], v159 offset:8800
	ds_read_b128 v[160:163], v159 offset:128
	s_waitcnt vmcnt(4) lgkmcnt(2)
	v_mfma_f32_32x32x16_f16 v[50:65], v[134:137], v[102:105], v[50:65]
	s_waitcnt lgkmcnt(1)
	v_mfma_f32_32x32x16_f16 v[34:49], v[130:133], v[102:105], v[34:49]
	v_mfma_f32_32x32x16_f16 v[2:17], v[134:137], v[98:101], v[2:17]
	v_mfma_f32_32x32x16_f16 v[18:33], v[130:133], v[98:101], v[18:33]
	ds_read_b128 v[130:133], v159 offset:8832
	ds_read_b128 v[134:137], v159 offset:160
	s_waitcnt vmcnt(3) lgkmcnt(2)
	v_mfma_f32_32x32x16_f16 v[50:65], v[160:163], v[94:97], v[50:65]
	s_waitcnt lgkmcnt(1)
	v_mfma_f32_32x32x16_f16 v[34:49], v[130:133], v[94:97], v[34:49]
	v_mfma_f32_32x32x16_f16 v[2:17], v[160:163], v[86:89], v[2:17]
	v_mfma_f32_32x32x16_f16 v[18:33], v[130:133], v[86:89], v[18:33]
	ds_read_b128 v[130:133], v159 offset:8864
	ds_read_b128 v[160:163], v159 offset:192
	s_waitcnt vmcnt(2) lgkmcnt(2)
	v_mfma_f32_32x32x16_f16 v[50:65], v[134:137], v[90:93], v[50:65]
	s_waitcnt lgkmcnt(1)
	v_mfma_f32_32x32x16_f16 v[34:49], v[130:133], v[90:93], v[34:49]
	v_mfma_f32_32x32x16_f16 v[2:17], v[134:137], v[78:81], v[2:17]
	v_mfma_f32_32x32x16_f16 v[18:33], v[130:133], v[78:81], v[18:33]
	ds_read_b128 v[130:133], v159 offset:8896
	ds_read_b128 v[164:167], v159 offset:224
	s_waitcnt vmcnt(1) lgkmcnt(2)
	v_mfma_f32_32x32x16_f16 v[50:65], v[160:163], v[82:85], v[50:65]
	s_waitcnt lgkmcnt(1)
	v_mfma_f32_32x32x16_f16 v[34:49], v[130:133], v[82:85], v[34:49]
	v_mfma_f32_32x32x16_f16 v[2:17], v[160:163], v[70:73], v[2:17]
	v_mfma_f32_32x32x16_f16 v[18:33], v[130:133], v[70:73], v[18:33]
	v_lshlrev_b32_e32 v130, 3, v138
	v_and_b32_e32 v168, 0x1f8, v130
	global_load_dwordx2 v[138:139], v168, s[0:1]
	global_load_dwordx2 v[134:135], v168, s[0:1] offset:512
	global_load_dwordx2 v[132:133], v168, s[0:1] offset:1024
	global_load_dwordx2 v[130:131], v168, s[0:1] offset:1536
	global_load_dwordx2 v[136:137], v168, s[0:1] offset:2048
	s_waitcnt vmcnt(5) lgkmcnt(0)
	v_mfma_f32_32x32x16_f16 v[50:65], v[164:167], v[74:77], v[50:65]
	v_mfma_f32_32x32x16_f16 v[2:17], v[164:167], v[66:69], v[2:17]
	s_nop 10
	v_cvt_pk_f16_f32 v57, v56, v57
	v_cvt_pk_f16_f32 v56, v54, v55
	v_cvt_pk_f16_f32 v55, v52, v53
	v_cvt_pk_f16_f32 v54, v50, v51
	v_perm_b32 v50, v240, v154, s42
	v_perm_b32 v51, v240, v154, s43
	v_perm_b32 v52, v240, v155, s42
	v_perm_b32 v53, v240, v155, s43
	v_pk_add_f16 v50, v50, s3 op_sel_hi:[1,0]
	v_pk_add_f16 v51, v51, s3 op_sel_hi:[1,0]
	v_pk_add_f16 v52, v52, s3 op_sel_hi:[1,0]
	v_pk_add_f16 v53, v53, s3 op_sel_hi:[1,0]
	v_cvt_pk_f16_f32 v65, v64, v65
	v_cvt_pk_f16_f32 v64, v62, v63
	v_cvt_pk_f16_f32 v63, v60, v61
	v_cvt_pk_f16_f32 v62, v58, v59
	v_mfma_f32_32x32x16_f16 v[2:17], v[50:53], v[54:57], v[2:17]
	v_perm_b32 v58, v240, v150, s42
	v_perm_b32 v59, v240, v150, s43
	v_perm_b32 v60, v240, v151, s42
	v_perm_b32 v61, v240, v151, s43
	v_pk_add_f16 v58, v58, s3 op_sel_hi:[1,0]
	v_pk_add_f16 v59, v59, s3 op_sel_hi:[1,0]
	v_pk_add_f16 v60, v60, s3 op_sel_hi:[1,0]
	v_pk_add_f16 v61, v61, s3 op_sel_hi:[1,0]
	s_nop 1
	v_mfma_f32_32x32x16_f16 v[2:17], v[58:61], v[62:65], v[2:17]
	ds_read_b128 v[160:163], v159 offset:8928
	v_perm_b32 v155, v240, v152, s43
	v_perm_b32 v164, v240, v153, s42
	s_waitcnt lgkmcnt(0)
	v_mfma_f32_32x32x16_f16 v[18:33], v[160:163], v[66:69], v[18:33]
	v_perm_b32 v154, v240, v152, s42
	v_perm_b32 v165, v240, v153, s43
	v_pk_add_f16 v152, v154, s3 op_sel_hi:[1,0]
	v_pk_add_f16 v153, v155, s3 op_sel_hi:[1,0]
	v_pk_add_f16 v154, v164, s3 op_sel_hi:[1,0]
	v_pk_add_f16 v155, v165, s3 op_sel_hi:[1,0]
	v_mfma_f32_32x32x16_f16 v[34:49], v[160:163], v[74:77], v[34:49]
	v_perm_b32 v151, v240, v148, s43
	v_perm_b32 v164, v240, v149, s42
	v_mfma_f32_32x32x16_f16 v[18:33], v[152:155], v[54:57], v[18:33]
	v_perm_b32 v150, v240, v148, s42
	v_perm_b32 v165, v240, v149, s43
	v_pk_add_f16 v148, v150, s3 op_sel_hi:[1,0]
	v_pk_add_f16 v149, v151, s3 op_sel_hi:[1,0]
	v_pk_add_f16 v150, v164, s3 op_sel_hi:[1,0]
	v_pk_add_f16 v151, v165, s3 op_sel_hi:[1,0]
	s_nop 2
	v_cvt_pk_f16_f32 v41, v40, v41
	v_cvt_pk_f16_f32 v40, v38, v39
	v_cvt_pk_f16_f32 v38, v34, v35
	v_cvt_pk_f16_f32 v39, v36, v37
	v_mfma_f32_32x32x16_f16 v[18:33], v[148:151], v[62:65], v[18:33]
	v_perm_b32 v34, v240, v146, s42
	v_perm_b32 v35, v240, v146, s43
	v_perm_b32 v36, v240, v147, s42
	v_perm_b32 v37, v240, v147, s43
	v_pk_add_f16 v34, v34, s3 op_sel_hi:[1,0]
	v_pk_add_f16 v35, v35, s3 op_sel_hi:[1,0]
	v_pk_add_f16 v36, v36, s3 op_sel_hi:[1,0]
	v_pk_add_f16 v37, v37, s3 op_sel_hi:[1,0]
	v_perm_b32 v146, v240, v144, s42
	v_perm_b32 v144, v240, v144, s43
	v_perm_b32 v147, v240, v145, s42
	v_perm_b32 v53, v240, v145, s43
	v_pk_add_f16 v50, v146, s3 op_sel_hi:[1,0]
	v_pk_add_f16 v51, v144, s3 op_sel_hi:[1,0]
	v_pk_add_f16 v52, v147, s3 op_sel_hi:[1,0]
	v_pk_add_f16 v53, v53, s3 op_sel_hi:[1,0]
	v_cvt_pk_f16_f32 v49, v48, v49
	v_cvt_pk_f16_f32 v48, v46, v47
	v_cvt_pk_f16_f32 v47, v44, v45
	v_mfma_f32_32x32x16_f16 v[2:17], v[34:37], v[38:41], v[2:17]
	v_cvt_pk_f16_f32 v46, v42, v43
	v_lshlrev_b32_e32 v54, 8, v140
	v_mfma_f32_32x32x16_f16 v[18:33], v[50:53], v[38:41], v[18:33]
	v_lshrrev_b32_e32 v37, 16, v141
	v_lshrrev_b32_e32 v38, 8, v141
	v_perm_b32 v34, v54, v140, s2
	v_perm_b32 v37, v38, v37, s2
	v_or_b32_e32 v34, 0x64006400, v34
	v_perm_b32 v35, v240, v140, s43
	v_perm_b32 v36, v240, v141, s42
	v_or_b32_e32 v37, 0x64006400, v37
	v_perm_b32 v42, v240, v142, s42
	v_perm_b32 v43, v240, v142, s43
	v_perm_b32 v44, v240, v143, s42
	v_perm_b32 v45, v240, v143, s43
	v_pk_add_f16 v34, v34, s3 op_sel_hi:[1,0]
	v_pk_add_f16 v35, v35, s3 op_sel_hi:[1,0]
	v_pk_add_f16 v36, v36, s3 op_sel_hi:[1,0]
	v_pk_add_f16 v37, v37, s3 op_sel_hi:[1,0]
	v_pk_add_f16 v42, v42, s3 op_sel_hi:[1,0]
	v_pk_add_f16 v43, v43, s3 op_sel_hi:[1,0]
	v_pk_add_f16 v44, v44, s3 op_sel_hi:[1,0]
	v_pk_add_f16 v45, v45, s3 op_sel_hi:[1,0]
	v_mfma_f32_32x32x16_f16 v[18:33], v[34:37], v[46:49], v[18:33]
	global_load_dwordx2 v[154:155], v168, s[0:1] offset:2560
	global_load_dwordx2 v[152:153], v168, s[0:1] offset:3072
	global_load_dwordx2 v[150:151], v168, s[0:1] offset:3584
	v_mov_b32_e32 v148, v0
	s_or_b32 s0, s10, 4
	s_ashr_i32 s1, s0, 31
	s_lshl_b64 s[0:1], s[0:1], 12
	v_mfma_f32_32x32x16_f16 v[2:17], v[42:45], v[46:49], v[2:17]
	s_nop 3
	v_add_f32_e32 v196, v157, v18
	v_mul_u32_u24_e32 v18, 0x120, v158
	v_lshl_add_u32 v158, v18, 1, v1
	v_cvt_f16_f32_e32 v1, v196
	v_add_f32_e32 v204, v157, v20
	v_add_f32_e32 v160, v157, v21
	v_add_f32_e32 v162, v157, v22
	s_nop 0
	v_add_f32_e32 v193, v157, v2
	v_add_f32_e32 v198, v157, v3
	v_cvt_pk_f16_f32 v2, v193, v198
	ds_write_b16 v158, v1 offset:4608
	v_add_f32_e32 v203, v157, v4
	v_add_f32_e32 v1, v157, v5
	ds_write_b16 v158, v2
	ds_write_b16_d16_hi v158, v2 offset:144
	v_cvt_pk_f16_f32 v2, v203, v204
	v_cvt_pk_f16_f32 v4, v1, v160
	v_add_f32_e32 v161, v157, v6
	v_add_f32_e32 v163, v157, v7
	v_add_f32_e32 v164, v157, v23
	ds_write_b16 v158, v2 offset:288
	ds_write_b16_d16_hi v158, v2 offset:4896
	ds_write_b16 v158, v4 offset:432
	ds_write_b16_d16_hi v158, v4 offset:5040
	v_cvt_pk_f16_f32 v2, v161, v162
	v_cvt_pk_f16_f32 v4, v163, v164
	v_add_f32_e32 v165, v157, v8
	v_add_f32_e32 v166, v157, v24
	v_add_f32_e32 v167, v157, v9
	v_add_f32_e32 v168, v157, v25
	ds_write_b16 v158, v2 offset:1152
	ds_write_b16_d16_hi v158, v2 offset:5760
	ds_write_b16 v158, v4 offset:1296
	ds_write_b16_d16_hi v158, v4 offset:5904
	v_cvt_pk_f16_f32 v2, v165, v166
	v_cvt_pk_f16_f32 v4, v167, v168
	v_add_f32_e32 v169, v157, v10
	v_add_f32_e32 v170, v157, v26
	v_add_f32_e32 v171, v157, v11
	v_add_f32_e32 v172, v157, v27
	ds_write_b16 v158, v2 offset:1440
	ds_write_b16_d16_hi v158, v2 offset:6048
	ds_write_b16 v158, v4 offset:1584
	ds_write_b16_d16_hi v158, v4 offset:6192
	v_cvt_pk_f16_f32 v2, v169, v170
	v_cvt_pk_f16_f32 v4, v171, v172
	v_add_f32_e32 v173, v157, v12
	v_add_f32_e32 v174, v157, v28
	v_add_f32_e32 v175, v157, v13
	v_add_f32_e32 v176, v157, v29
	ds_write_b16 v158, v2 offset:2304
	ds_write_b16_d16_hi v158, v2 offset:6912
	ds_write_b16 v158, v4 offset:2448
	ds_write_b16_d16_hi v158, v4 offset:7056
	v_cvt_pk_f16_f32 v2, v173, v174
	v_cvt_pk_f16_f32 v4, v175, v176
	v_add_f32_e32 v177, v157, v14
	v_add_f32_e32 v178, v157, v30
	v_add_f32_e32 v179, v157, v15
	v_add_f32_e32 v180, v157, v31
	ds_write_b16 v158, v2 offset:2592
	ds_write_b16_d16_hi v158, v2 offset:7200
	ds_write_b16 v158, v4 offset:2736
	ds_write_b16_d16_hi v158, v4 offset:7344
	v_cvt_pk_f16_f32 v2, v177, v178
	v_cvt_pk_f16_f32 v4, v179, v180
	v_add_f32_e32 v200, v157, v19
	v_add_f32_e32 v181, v157, v16
	v_add_f32_e32 v183, v157, v32
	v_add_f32_e32 v182, v157, v17
	v_add_f32_e32 v184, v157, v33
	v_cvt_pk_f16_f32 v18, v200, v181
	ds_write_b16 v158, v2 offset:3456
	ds_write_b16_d16_hi v158, v2 offset:8064
	ds_write_b16 v158, v4 offset:3600
	ds_write_b16_d16_hi v158, v4 offset:8208
	v_cvt_pk_f16_f32 v3, v183, v182
	v_cvt_f16_f32_e32 v5, v184
	ds_write_b16 v158, v18 offset:4752
	ds_write_b16_d16_hi v158, v18 offset:3744
	ds_write_b16 v158, v3 offset:8352
	ds_write_b16_d16_hi v158, v3 offset:3888
	ds_write_b16 v158, v5 offset:8496
	s_waitcnt lgkmcnt(0)
	s_barrier
	ds_read_b128 v[2:5], v159 offset:34816
	ds_read_b128 v[18:21], v159 offset:43520
	ds_read_b128 v[140:143], v159 offset:34848
	ds_read_b128 v[144:147], v159 offset:43552
	s_waitcnt lgkmcnt(3)
	v_mfma_f32_32x32x16_f16 v[50:65], v[2:5], v[126:129], 0
	s_add_u32 s0, s8, s0
	s_addc_u32 s1, s9, s1
	s_waitcnt lgkmcnt(2)
	v_mfma_f32_32x32x16_f16 v[34:49], v[18:21], v[126:129], 0
	v_mfma_f32_32x32x16_f16 v[2:17], v[2:5], v[122:125], 0
	v_mfma_f32_32x32x16_f16 v[18:33], v[18:21], v[122:125], 0
	ds_read_b128 v[242:245], v159 offset:34880
	ds_read_b128 v[246:249], v159 offset:43584
	s_waitcnt lgkmcnt(3)
	v_mfma_f32_32x32x16_f16 v[50:65], v[140:143], v[118:121], v[50:65]
	s_waitcnt lgkmcnt(2)
	v_mfma_f32_32x32x16_f16 v[34:49], v[144:147], v[118:121], v[34:49]
	v_mfma_f32_32x32x16_f16 v[2:17], v[140:143], v[114:117], v[2:17]
	v_mfma_f32_32x32x16_f16 v[18:33], v[144:147], v[114:117], v[18:33]
	ds_read_b128 v[140:143], v159 offset:34912
	ds_read_b128 v[144:147], v159 offset:43616
	s_waitcnt lgkmcnt(3)
	v_mfma_f32_32x32x16_f16 v[50:65], v[242:245], v[110:113], v[50:65]
	s_waitcnt lgkmcnt(2)
	v_mfma_f32_32x32x16_f16 v[34:49], v[246:249], v[110:113], v[34:49]
	v_mfma_f32_32x32x16_f16 v[2:17], v[242:245], v[106:109], v[2:17]
	v_mfma_f32_32x32x16_f16 v[18:33], v[246:249], v[106:109], v[18:33]
	ds_read_b128 v[242:245], v159 offset:34944
	ds_read_b128 v[246:249], v159 offset:43648
	s_waitcnt lgkmcnt(3)
	v_mfma_f32_32x32x16_f16 v[50:65], v[140:143], v[102:105], v[50:65]
	s_waitcnt lgkmcnt(2)
	v_mfma_f32_32x32x16_f16 v[34:49], v[144:147], v[102:105], v[34:49]
	v_mfma_f32_32x32x16_f16 v[2:17], v[140:143], v[98:101], v[2:17]
	v_mfma_f32_32x32x16_f16 v[18:33], v[144:147], v[98:101], v[18:33]
	ds_read_b128 v[186:189], v159 offset:34976
	ds_read_b128 v[206:209], v159 offset:43680
	s_waitcnt lgkmcnt(3)
	v_mfma_f32_32x32x16_f16 v[50:65], v[242:245], v[94:97], v[50:65]
	s_waitcnt lgkmcnt(2)
	v_mfma_f32_32x32x16_f16 v[34:49], v[246:249], v[94:97], v[34:49]
	v_mfma_f32_32x32x16_f16 v[2:17], v[242:245], v[86:89], v[2:17]
	v_mfma_f32_32x32x16_f16 v[18:33], v[246:249], v[86:89], v[18:33]
	ds_read_b128 v[140:143], v159 offset:35008
	ds_read_b128 v[144:147], v159 offset:43712
	s_waitcnt lgkmcnt(3)
	v_mfma_f32_32x32x16_f16 v[50:65], v[186:189], v[90:93], v[50:65]
	s_waitcnt lgkmcnt(2)
	v_mfma_f32_32x32x16_f16 v[34:49], v[206:209], v[90:93], v[34:49]
	v_mfma_f32_32x32x16_f16 v[2:17], v[186:189], v[78:81], v[2:17]
	v_mfma_f32_32x32x16_f16 v[18:33], v[206:209], v[78:81], v[18:33]
	ds_read_b128 v[186:189], v159 offset:35040
	ds_read_b128 v[206:209], v159 offset:43744
	s_waitcnt lgkmcnt(3)
	v_mfma_f32_32x32x16_f16 v[50:65], v[140:143], v[82:85], v[50:65]
	s_waitcnt lgkmcnt(2)
	v_mfma_f32_32x32x16_f16 v[34:49], v[144:147], v[82:85], v[34:49]
	v_mfma_f32_32x32x16_f16 v[2:17], v[140:143], v[70:73], v[2:17]
	v_lshlrev_b32_e32 v140, 3, v148
	v_and_b32_e32 v185, 0x1f8, v140
	global_load_dwordx2 v[148:149], v185, s[0:1]
	global_load_dwordx2 v[142:143], v185, s[0:1] offset:1024
	global_load_dwordx2 v[140:141], v185, s[0:1] offset:1536
	v_mfma_f32_32x32x16_f16 v[18:33], v[144:147], v[70:73], v[18:33]
	global_load_dwordx2 v[144:145], v185, s[0:1] offset:512
	global_load_dwordx2 v[146:147], v185, s[0:1] offset:2048
	s_waitcnt lgkmcnt(1)
	v_mfma_f32_32x32x16_f16 v[50:65], v[186:189], v[74:77], v[50:65]
	v_mfma_f32_32x32x16_f16 v[2:17], v[186:189], v[66:69], v[2:17]
	s_nop 10
	v_cvt_pk_f16_f32 v57, v56, v57
	v_cvt_pk_f16_f32 v56, v54, v55
	v_cvt_pk_f16_f32 v54, v50, v51
	s_waitcnt vmcnt(12)
	v_cvt_pk_f16_f32 v55, v52, v53
	s_waitcnt vmcnt(8)
	v_perm_b32 v50, v240, v138, s42
	v_perm_b32 v51, v240, v138, s43
	v_perm_b32 v52, v240, v139, s42
	v_perm_b32 v53, v240, v139, s43
	v_perm_b32 v139, v240, v136, s43
	v_pk_add_f16 v50, v50, s3 op_sel_hi:[1,0]
	v_pk_add_f16 v51, v51, s3 op_sel_hi:[1,0]
	v_pk_add_f16 v52, v52, s3 op_sel_hi:[1,0]
	v_pk_add_f16 v53, v53, s3 op_sel_hi:[1,0]
	v_perm_b32 v190, v240, v137, s42
	s_waitcnt lgkmcnt(0)
	v_mfma_f32_32x32x16_f16 v[18:33], v[206:209], v[66:69], v[18:33]
	v_perm_b32 v138, v240, v136, s42
	v_perm_b32 v191, v240, v137, s43
	v_pk_add_f16 v136, v138, s3 op_sel_hi:[1,0]
	v_pk_add_f16 v137, v139, s3 op_sel_hi:[1,0]
	v_pk_add_f16 v138, v190, s3 op_sel_hi:[1,0]
	v_pk_add_f16 v139, v191, s3 op_sel_hi:[1,0]
	v_cvt_pk_f16_f32 v65, v64, v65
	v_cvt_pk_f16_f32 v64, v62, v63
	v_cvt_pk_f16_f32 v63, v60, v61
	v_cvt_pk_f16_f32 v62, v58, v59
	v_mfma_f32_32x32x16_f16 v[34:49], v[206:209], v[74:77], v[34:49]
	v_mfma_f32_32x32x16_f16 v[2:17], v[50:53], v[54:57], v[2:17]
	s_waitcnt vmcnt(7)
	v_perm_b32 v58, v240, v134, s42
	v_perm_b32 v59, v240, v134, s43
	v_perm_b32 v60, v240, v135, s42
	v_perm_b32 v61, v240, v135, s43
	v_pk_add_f16 v58, v58, s3 op_sel_hi:[1,0]
	v_pk_add_f16 v59, v59, s3 op_sel_hi:[1,0]
	v_pk_add_f16 v60, v60, s3 op_sel_hi:[1,0]
	v_pk_add_f16 v61, v61, s3 op_sel_hi:[1,0]
	v_mfma_f32_32x32x16_f16 v[18:33], v[136:139], v[54:57], v[18:33]
	v_perm_b32 v134, v240, v154, s42
	v_perm_b32 v135, v240, v154, s43
	v_perm_b32 v154, v240, v155, s42
	v_perm_b32 v155, v240, v155, s43
	v_pk_add_f16 v210, v134, s3 op_sel_hi:[1,0]
	v_pk_add_f16 v211, v135, s3 op_sel_hi:[1,0]
	v_pk_add_f16 v212, v154, s3 op_sel_hi:[1,0]
	v_pk_add_f16 v213, v155, s3 op_sel_hi:[1,0]
	v_cvt_pk_f16_f32 v41, v40, v41
	v_cvt_pk_f16_f32 v40, v38, v39
	v_cvt_pk_f16_f32 v39, v36, v37
	v_cvt_pk_f16_f32 v38, v34, v35
	v_mfma_f32_32x32x16_f16 v[2:17], v[58:61], v[62:65], v[2:17]
	v_perm_b32 v34, v240, v132, s42
	v_perm_b32 v35, v240, v132, s43
	v_perm_b32 v36, v240, v133, s42
	v_perm_b32 v37, v240, v133, s43
	v_pk_add_f16 v34, v34, s3 op_sel_hi:[1,0]
	v_pk_add_f16 v35, v35, s3 op_sel_hi:[1,0]
	v_pk_add_f16 v36, v36, s3 op_sel_hi:[1,0]
	v_pk_add_f16 v37, v37, s3 op_sel_hi:[1,0]
	s_waitcnt vmcnt(6)
	v_mfma_f32_32x32x16_f16 v[18:33], v[210:213], v[62:65], v[18:33]
	v_perm_b32 v132, v240, v152, s42
	v_perm_b32 v133, v240, v152, s43
	v_perm_b32 v134, v240, v153, s42
	v_perm_b32 v53, v240, v153, s43
	v_pk_add_f16 v50, v132, s3 op_sel_hi:[1,0]
	v_pk_add_f16 v51, v133, s3 op_sel_hi:[1,0]
	v_pk_add_f16 v52, v134, s3 op_sel_hi:[1,0]
	v_pk_add_f16 v53, v53, s3 op_sel_hi:[1,0]
	v_cvt_pk_f16_f32 v49, v48, v49
	v_cvt_pk_f16_f32 v48, v46, v47
	v_cvt_pk_f16_f32 v47, v44, v45
	v_cvt_pk_f16_f32 v46, v42, v43
	v_mfma_f32_32x32x16_f16 v[2:17], v[34:37], v[38:41], v[2:17]
	v_perm_b32 v42, v240, v130, s42
	v_perm_b32 v43, v240, v130, s43
	v_perm_b32 v44, v240, v131, s42
	v_perm_b32 v45, v240, v131, s43
	v_pk_add_f16 v42, v42, s3 op_sel_hi:[1,0]
	v_pk_add_f16 v43, v43, s3 op_sel_hi:[1,0]
	v_pk_add_f16 v44, v44, s3 op_sel_hi:[1,0]
	v_pk_add_f16 v45, v45, s3 op_sel_hi:[1,0]
	s_waitcnt vmcnt(5)
	v_lshlrev_b32_e32 v54, 8, v150
	v_mfma_f32_32x32x16_f16 v[18:33], v[50:53], v[38:41], v[18:33]
	v_lshrrev_b32_e32 v37, 16, v151
	v_lshrrev_b32_e32 v38, 8, v151
	v_perm_b32 v34, v54, v150, s2
	v_perm_b32 v37, v38, v37, s2
	v_or_b32_e32 v34, 0x64006400, v34
	v_perm_b32 v35, v240, v150, s43
	v_perm_b32 v36, v240, v151, s42
	v_or_b32_e32 v37, 0x64006400, v37
	v_pk_add_f16 v34, v34, s3 op_sel_hi:[1,0]
	v_pk_add_f16 v35, v35, s3 op_sel_hi:[1,0]
	v_pk_add_f16 v36, v36, s3 op_sel_hi:[1,0]
	v_pk_add_f16 v37, v37, s3 op_sel_hi:[1,0]
	v_mfma_f32_32x32x16_f16 v[2:17], v[42:45], v[46:49], v[2:17]
	global_load_dwordx2 v[154:155], v185, s[0:1] offset:2560
	global_load_dwordx2 v[152:153], v185, s[0:1] offset:3072
	global_load_dwordx2 v[150:151], v185, s[0:1] offset:3584
	s_or_b32 s0, s10, 6
	s_ashr_i32 s1, s0, 31
	s_lshl_b64 s[0:1], s[0:1], 12
	s_add_u32 s0, s8, s0
	v_mfma_f32_32x32x16_f16 v[18:33], v[34:37], v[46:49], v[18:33]
	s_nop 3
	v_add_f32_e32 v185, v157, v2
	v_add_f32_e32 v187, v157, v3
	v_cvt_pk_f16_f32 v2, v185, v187
	v_add_f32_e32 v189, v157, v4
	v_add_f32_e32 v191, v157, v5
	ds_write_b16 v158, v2 offset:18432
	s_nop 0
	s_nop 0
	v_add_f32_e32 v190, v157, v20
	v_add_f32_e32 v192, v157, v21
	ds_write_b16_d16_hi v158, v2 offset:18576
	v_cvt_pk_f16_f32 v2, v189, v190
	v_cvt_pk_f16_f32 v4, v191, v192
	v_add_f32_e32 v194, v157, v6
	v_add_f32_e32 v195, v157, v22
	v_add_f32_e32 v197, v157, v7
	v_add_f32_e32 v199, v157, v23
	ds_write_b16 v158, v2 offset:18720
	ds_write_b16_d16_hi v158, v2 offset:23328
	ds_write_b16 v158, v4 offset:18864
	ds_write_b16_d16_hi v158, v4 offset:23472
	v_cvt_pk_f16_f32 v2, v194, v195
	v_cvt_pk_f16_f32 v4, v197, v199
	v_add_f32_e32 v201, v157, v8
	v_add_f32_e32 v202, v157, v24
	v_add_f32_e32 v205, v157, v9
	v_add_f32_e32 v206, v157, v25
	ds_write_b16 v158, v2 offset:19584
	ds_write_b16_d16_hi v158, v2 offset:24192
	ds_write_b16 v158, v4 offset:19728
	ds_write_b16_d16_hi v158, v4 offset:24336
	v_cvt_pk_f16_f32 v2, v201, v202
	v_cvt_pk_f16_f32 v4, v205, v206
	v_add_f32_e32 v207, v157, v10
	v_add_f32_e32 v209, v157, v26
	v_add_f32_e32 v208, v157, v11
	v_add_f32_e32 v210, v157, v27
	ds_write_b16 v158, v2 offset:19872
	ds_write_b16_d16_hi v158, v2 offset:24480
	ds_write_b16 v158, v4 offset:20016
	ds_write_b16_d16_hi v158, v4 offset:24624
	v_cvt_pk_f16_f32 v2, v207, v209
	v_cvt_pk_f16_f32 v4, v208, v210
	v_add_f32_e32 v211, v157, v12
	v_add_f32_e32 v212, v157, v28
	v_add_f32_e32 v213, v157, v13
	v_add_f32_e32 v214, v157, v29
	ds_write_b16 v158, v2 offset:20736
	ds_write_b16_d16_hi v158, v2 offset:25344
	ds_write_b16 v158, v4 offset:20880
	ds_write_b16_d16_hi v158, v4 offset:25488
	v_cvt_pk_f16_f32 v2, v211, v212
	v_cvt_pk_f16_f32 v4, v213, v214
	v_add_f32_e32 v215, v157, v14
	v_add_f32_e32 v216, v157, v30
	v_add_f32_e32 v217, v157, v15
	v_add_f32_e32 v218, v157, v31
	ds_write_b16 v158, v2 offset:21024
	ds_write_b16_d16_hi v158, v2 offset:25632
	ds_write_b16 v158, v4 offset:21168
	ds_write_b16_d16_hi v158, v4 offset:25776
	v_cvt_pk_f16_f32 v2, v215, v216
	v_cvt_pk_f16_f32 v4, v217, v218
	v_add_f32_e32 v186, v157, v18
	v_add_f32_e32 v188, v157, v19
	v_add_f32_e32 v219, v157, v16
	v_add_f32_e32 v221, v157, v32
	v_add_f32_e32 v220, v157, v17
	v_add_f32_e32 v222, v157, v33
	v_cvt_pk_f16_f32 v18, v186, v188
	ds_write_b16 v158, v2 offset:21888
	ds_write_b16_d16_hi v158, v2 offset:26496
	ds_write_b16 v158, v4 offset:22032
	ds_write_b16_d16_hi v158, v4 offset:26640
	v_cvt_pk_f16_f32 v2, v219, v221
	v_cvt_pk_f16_f32 v4, v220, v222
	ds_write_b16 v158, v18 offset:23040
	ds_write_b16_d16_hi v158, v18 offset:23184
	ds_write_b16 v158, v2 offset:22176
	ds_write_b16_d16_hi v158, v2 offset:26784
	ds_write_b16 v158, v4 offset:22320
	ds_write_b16_d16_hi v158, v4 offset:26928
	s_waitcnt lgkmcnt(0)
	s_barrier
	ds_read_b128 v[2:5], v159
	ds_read_b128 v[18:21], v159 offset:8704
	s_waitcnt lgkmcnt(1)
	v_mfma_f32_32x32x16_f16 v[50:65], v[2:5], v[126:129], 0
	v_lshlrev_b32_e32 v0, 3, v0
	s_addc_u32 s1, s9, s1
	v_and_b32_e32 v0, 0x1f8, v0
	global_load_dwordx2 v[138:139], v0, s[0:1]
	s_waitcnt lgkmcnt(0)
	v_mfma_f32_32x32x16_f16 v[34:49], v[18:21], v[126:129], 0
	v_mfma_f32_32x32x16_f16 v[2:17], v[2:5], v[122:125], 0
	v_mfma_f32_32x32x16_f16 v[18:33], v[18:21], v[122:125], 0
	ds_read_b128 v[130:133], v159 offset:32
	ds_read_b128 v[134:137], v159 offset:8736
	s_waitcnt lgkmcnt(1)
	v_mfma_f32_32x32x16_f16 v[50:65], v[130:133], v[118:121], v[50:65]
	s_waitcnt lgkmcnt(0)
	v_mfma_f32_32x32x16_f16 v[34:49], v[134:137], v[118:121], v[34:49]
	v_mfma_f32_32x32x16_f16 v[2:17], v[130:133], v[114:117], v[2:17]
	v_mfma_f32_32x32x16_f16 v[18:33], v[134:137], v[114:117], v[18:33]
	ds_read_b128 v[224:227], v159 offset:64
	ds_read_b128 v[228:231], v159 offset:8768
	ds_read_b128 v[130:133], v159 offset:96
	ds_read_b128 v[134:137], v159 offset:8800
	s_waitcnt lgkmcnt(3)
	v_mfma_f32_32x32x16_f16 v[50:65], v[224:227], v[110:113], v[50:65]
	s_waitcnt lgkmcnt(2)
	v_mfma_f32_32x32x16_f16 v[34:49], v[228:231], v[110:113], v[34:49]
	v_mfma_f32_32x32x16_f16 v[2:17], v[224:227], v[106:109], v[2:17]
	v_mfma_f32_32x32x16_f16 v[18:33], v[228:231], v[106:109], v[18:33]
	ds_read_b128 v[224:227], v159 offset:128
	ds_read_b128 v[228:231], v159 offset:8832
	s_waitcnt lgkmcnt(3)
	v_mfma_f32_32x32x16_f16 v[50:65], v[130:133], v[102:105], v[50:65]
	s_waitcnt lgkmcnt(2)
	v_mfma_f32_32x32x16_f16 v[34:49], v[134:137], v[102:105], v[34:49]
	v_mfma_f32_32x32x16_f16 v[2:17], v[130:133], v[98:101], v[2:17]
	v_mfma_f32_32x32x16_f16 v[18:33], v[134:137], v[98:101], v[18:33]
	ds_read_b128 v[130:133], v159 offset:160
	ds_read_b128 v[134:137], v159 offset:8864
	s_waitcnt lgkmcnt(3)
	v_mfma_f32_32x32x16_f16 v[50:65], v[224:227], v[94:97], v[50:65]
	s_waitcnt lgkmcnt(2)
	v_mfma_f32_32x32x16_f16 v[34:49], v[228:231], v[94:97], v[34:49]
	v_mfma_f32_32x32x16_f16 v[2:17], v[224:227], v[86:89], v[2:17]
	v_mfma_f32_32x32x16_f16 v[18:33], v[228:231], v[86:89], v[18:33]
	ds_read_b128 v[224:227], v159 offset:192
	ds_read_b128 v[228:231], v159 offset:8896
	s_waitcnt lgkmcnt(3)
	v_mfma_f32_32x32x16_f16 v[50:65], v[130:133], v[90:93], v[50:65]
	s_waitcnt lgkmcnt(2)
	v_mfma_f32_32x32x16_f16 v[34:49], v[134:137], v[90:93], v[34:49]
	v_mfma_f32_32x32x16_f16 v[2:17], v[130:133], v[78:81], v[2:17]
	v_add_f32_e32 v130, v193, v196
	v_add_f32_e32 v130, 0, v130
	v_add_f32_e32 v132, v198, v200
	v_add_f32_e32 v130, v132, v130
	v_mul_f32_e32 v132, v200, v200
	v_fmac_f32_e32 v132, v198, v198
	v_mul_f32_e32 v131, v196, v196
	v_mfma_f32_32x32x16_f16 v[18:33], v[134:137], v[78:81], v[18:33]
	ds_read_b128 v[232:235], v159 offset:224
	ds_read_b128 v[236:239], v159 offset:8928
	v_fmac_f32_e32 v131, v193, v193
	v_add_f32_e32 v131, v131, v132
	v_add_f32_e32 v132, v203, v204
	v_add_f32_e32 v130, v132, v130
	v_mul_f32_e32 v132, v204, v204
	s_waitcnt lgkmcnt(3)
	v_mfma_f32_32x32x16_f16 v[50:65], v[224:227], v[82:85], v[50:65]
	v_fmac_f32_e32 v132, v203, v203
	v_add_f32_e32 v193, v132, v131
	v_add_f32_e32 v131, v1, v160
	v_add_f32_e32 v196, v131, v130
	global_load_dwordx2 v[134:135], v0, s[0:1] offset:512
	global_load_dwordx2 v[132:133], v0, s[0:1] offset:1024
	global_load_dwordx2 v[130:131], v0, s[0:1] offset:1536
	s_waitcnt lgkmcnt(2)
	v_mfma_f32_32x32x16_f16 v[34:49], v[228:231], v[82:85], v[34:49]
	global_load_dwordx2 v[136:137], v0, s[0:1] offset:2048
	v_mfma_f32_32x32x16_f16 v[2:17], v[224:227], v[70:73], v[2:17]
	v_mfma_f32_32x32x16_f16 v[18:33], v[228:231], v[70:73], v[18:33]
	s_waitcnt lgkmcnt(1)
	v_mfma_f32_32x32x16_f16 v[50:65], v[232:235], v[74:77], v[50:65]
	v_mfma_f32_32x32x16_f16 v[2:17], v[232:235], v[66:69], v[2:17]
	s_nop 10
	v_cvt_pk_f16_f32 v57, v56, v57
	v_cvt_pk_f16_f32 v56, v54, v55
	v_cvt_pk_f16_f32 v54, v50, v51
	s_waitcnt vmcnt(12)
	v_lshlrev_b32_e32 v50, 8, v148
	v_cvt_pk_f16_f32 v55, v52, v53
	v_perm_b32 v50, v50, v148, s2
	v_lshrrev_b32_e32 v51, 16, v148
	v_lshrrev_b32_e32 v52, 8, v148
	v_lshrrev_b32_e32 v53, 16, v149
	v_lshrrev_b32_e32 v148, 8, v149
	v_perm_b32 v51, v52, v51, s2
	v_lshlrev_b32_e32 v52, 8, v149
	v_perm_b32 v53, v148, v53, s2
	s_waitcnt vmcnt(8)
	v_perm_b32 v52, v52, v149, s2
	v_perm_b32 v149, v240, v146, s43
	v_perm_b32 v198, v240, v147, s42
	s_waitcnt lgkmcnt(0)
	v_mfma_f32_32x32x16_f16 v[18:33], v[236:239], v[66:69], v[18:33]
	v_or_b32_e32 v50, 0x64006400, v50
	v_or_b32_e32 v51, 0x64006400, v51
	v_or_b32_e32 v52, 0x64006400, v52
	v_or_b32_e32 v53, 0x64006400, v53
	v_pk_add_f16 v50, v50, s3 op_sel_hi:[1,0]
	v_pk_add_f16 v51, v51, s3 op_sel_hi:[1,0]
	v_pk_add_f16 v52, v52, s3 op_sel_hi:[1,0]
	v_pk_add_f16 v53, v53, s3 op_sel_hi:[1,0]
	v_perm_b32 v148, v240, v146, s42
	v_perm_b32 v200, v240, v147, s43
	v_pk_add_f16 v146, v148, s3 op_sel_hi:[1,0]
	v_pk_add_f16 v147, v149, s3 op_sel_hi:[1,0]
	v_pk_add_f16 v148, v198, s3 op_sel_hi:[1,0]
	v_pk_add_f16 v149, v200, s3 op_sel_hi:[1,0]
	v_cvt_pk_f16_f32 v65, v64, v65
	v_cvt_pk_f16_f32 v64, v62, v63
	v_cvt_pk_f16_f32 v62, v58, v59
	v_cvt_pk_f16_f32 v63, v60, v61
	s_waitcnt vmcnt(7)
	v_mfma_f32_32x32x16_f16 v[34:49], v[236:239], v[74:77], v[34:49]
	v_mfma_f32_32x32x16_f16 v[2:17], v[50:53], v[54:57], v[2:17]
	v_perm_b32 v58, v240, v144, s42
	v_perm_b32 v59, v240, v144, s43
	v_perm_b32 v60, v240, v145, s42
	v_perm_b32 v61, v240, v145, s43
	v_mfma_f32_32x32x16_f16 v[18:33], v[146:149], v[54:57], v[18:33]
	v_pk_add_f16 v58, v58, s3 op_sel_hi:[1,0]
	v_pk_add_f16 v59, v59, s3 op_sel_hi:[1,0]
	v_pk_add_f16 v60, v60, s3 op_sel_hi:[1,0]
	v_pk_add_f16 v61, v61, s3 op_sel_hi:[1,0]
	v_perm_b32 v144, v240, v154, s42
	v_perm_b32 v145, v240, v154, s43
	v_perm_b32 v154, v240, v155, s42
	v_perm_b32 v155, v240, v155, s43
	v_pk_add_f16 v224, v144, s3 op_sel_hi:[1,0]
	v_pk_add_f16 v225, v145, s3 op_sel_hi:[1,0]
	v_pk_add_f16 v226, v154, s3 op_sel_hi:[1,0]
	v_pk_add_f16 v227, v155, s3 op_sel_hi:[1,0]
	v_cvt_pk_f16_f32 v41, v40, v41
	v_cvt_pk_f16_f32 v40, v38, v39
	v_cvt_pk_f16_f32 v39, v36, v37
	v_cvt_pk_f16_f32 v38, v34, v35
	s_waitcnt vmcnt(6)
	v_mfma_f32_32x32x16_f16 v[2:17], v[58:61], v[62:65], v[2:17]
	v_perm_b32 v34, v240, v142, s42
	v_perm_b32 v35, v240, v142, s43
	v_mfma_f32_32x32x16_f16 v[18:33], v[224:227], v[62:65], v[18:33]
	v_perm_b32 v36, v240, v143, s42
	v_perm_b32 v37, v240, v143, s43
	v_pk_add_f16 v34, v34, s3 op_sel_hi:[1,0]
	v_pk_add_f16 v35, v35, s3 op_sel_hi:[1,0]
	v_pk_add_f16 v36, v36, s3 op_sel_hi:[1,0]
	v_pk_add_f16 v37, v37, s3 op_sel_hi:[1,0]
	v_perm_b32 v142, v240, v152, s42
	v_perm_b32 v143, v240, v152, s43
	v_perm_b32 v144, v240, v153, s42
	v_perm_b32 v53, v240, v153, s43
	v_pk_add_f16 v50, v142, s3 op_sel_hi:[1,0]
	v_pk_add_f16 v51, v143, s3 op_sel_hi:[1,0]
	v_pk_add_f16 v52, v144, s3 op_sel_hi:[1,0]
	v_pk_add_f16 v53, v53, s3 op_sel_hi:[1,0]
	v_cvt_pk_f16_f32 v49, v48, v49
	v_cvt_pk_f16_f32 v48, v46, v47
	v_cvt_pk_f16_f32 v47, v44, v45
	v_cvt_pk_f16_f32 v46, v42, v43
	v_mfma_f32_32x32x16_f16 v[2:17], v[34:37], v[38:41], v[2:17]
	s_waitcnt vmcnt(5)
	v_lshlrev_b32_e32 v54, 8, v150
	v_mfma_f32_32x32x16_f16 v[18:33], v[50:53], v[38:41], v[18:33]
	v_lshrrev_b32_e32 v37, 16, v151
	v_lshrrev_b32_e32 v38, 8, v151
	v_perm_b32 v34, v54, v150, s2
	v_perm_b32 v37, v38, v37, s2
	v_perm_b32 v42, v240, v140, s42
	v_perm_b32 v43, v240, v140, s43
	v_perm_b32 v44, v240, v141, s42
	v_perm_b32 v45, v240, v141, s43
	v_or_b32_e32 v34, 0x64006400, v34
	v_perm_b32 v35, v240, v150, s43
	v_perm_b32 v36, v240, v151, s42
	v_or_b32_e32 v37, 0x64006400, v37
	v_pk_add_f16 v42, v42, s3 op_sel_hi:[1,0]
	v_pk_add_f16 v43, v43, s3 op_sel_hi:[1,0]
	v_pk_add_f16 v44, v44, s3 op_sel_hi:[1,0]
	v_pk_add_f16 v45, v45, s3 op_sel_hi:[1,0]
	v_pk_add_f16 v34, v34, s3 op_sel_hi:[1,0]
	v_pk_add_f16 v35, v35, s3 op_sel_hi:[1,0]
	v_pk_add_f16 v36, v36, s3 op_sel_hi:[1,0]
	v_pk_add_f16 v37, v37, s3 op_sel_hi:[1,0]
	v_mfma_f32_32x32x16_f16 v[2:17], v[42:45], v[46:49], v[2:17]
	global_load_dwordx2 v[142:143], v0, s[0:1] offset:2560
	global_load_dwordx2 v[140:141], v0, s[0:1] offset:3072
	global_load_dwordx2 v[64:65], v0, s[0:1] offset:3584
	v_mfma_f32_32x32x16_f16 v[18:33], v[34:37], v[46:49], v[18:33]
	s_nop 7
	v_add_f32_e32 v146, v157, v2
	v_add_f32_e32 v148, v157, v3
	v_cvt_pk_f16_f32 v0, v146, v148
	v_add_f32_e32 v150, v157, v4
	v_add_f32_e32 v152, v157, v5
	ds_write_b16 v158, v0
	v_add_f32_e32 v147, v157, v18
	v_cvt_f16_f32_e32 v2, v147
	v_add_f32_e32 v151, v157, v20
	v_add_f32_e32 v153, v157, v21
	ds_write_b16_d16_hi v158, v0 offset:144
	ds_write_b16 v158, v2 offset:4608
	v_cvt_pk_f16_f32 v0, v150, v151
	v_cvt_pk_f16_f32 v3, v152, v153
	v_add_f32_e32 v154, v157, v6
	v_add_f32_e32 v155, v157, v22
	v_add_f32_e32 v198, v157, v7
	v_add_f32_e32 v200, v157, v23
	ds_write_b16 v158, v0 offset:288
	ds_write_b16_d16_hi v158, v0 offset:4896
	ds_write_b16 v158, v3 offset:432
	ds_write_b16_d16_hi v158, v3 offset:5040
	v_cvt_pk_f16_f32 v0, v154, v155
	v_cvt_pk_f16_f32 v3, v198, v200
	v_add_f32_e32 v203, v157, v8
	v_add_f32_e32 v204, v157, v24
	v_add_f32_e32 v223, v157, v9
	v_add_f32_e32 v224, v157, v25
	ds_write_b16 v158, v0 offset:1152
	ds_write_b16_d16_hi v158, v0 offset:5760
	ds_write_b16 v158, v3 offset:1296
	ds_write_b16_d16_hi v158, v3 offset:5904
	v_cvt_pk_f16_f32 v0, v203, v204
	v_cvt_pk_f16_f32 v3, v223, v224
	v_add_f32_e32 v225, v157, v10
	v_add_f32_e32 v226, v157, v26
	v_add_f32_e32 v227, v157, v11
	v_add_f32_e32 v228, v157, v27
	ds_write_b16 v158, v0 offset:1440
	ds_write_b16_d16_hi v158, v0 offset:6048
	ds_write_b16 v158, v3 offset:1584
	ds_write_b16_d16_hi v158, v3 offset:6192
	v_cvt_pk_f16_f32 v0, v225, v226
	v_cvt_pk_f16_f32 v3, v227, v228
	v_add_f32_e32 v229, v157, v12
	v_add_f32_e32 v230, v157, v28
	v_add_f32_e32 v231, v157, v13
	v_add_f32_e32 v232, v157, v29
	ds_write_b16 v158, v0 offset:2304
	ds_write_b16_d16_hi v158, v0 offset:6912
	ds_write_b16 v158, v3 offset:2448
	ds_write_b16_d16_hi v158, v3 offset:7056
	v_cvt_pk_f16_f32 v0, v229, v230
	v_cvt_pk_f16_f32 v3, v231, v232
	v_add_f32_e32 v233, v157, v14
	v_add_f32_e32 v234, v157, v30
	v_add_f32_e32 v235, v157, v15
	v_add_f32_e32 v236, v157, v31
	ds_write_b16 v158, v0 offset:2592
	ds_write_b16_d16_hi v158, v0 offset:7200
	ds_write_b16 v158, v3 offset:2736
	ds_write_b16_d16_hi v158, v3 offset:7344
	v_cvt_pk_f16_f32 v0, v233, v234
	v_cvt_pk_f16_f32 v3, v235, v236
	v_add_f32_e32 v149, v157, v19
	v_add_f32_e32 v237, v157, v16
	v_add_f32_e32 v238, v157, v32
	v_add_f32_e32 v144, v157, v17
	v_add_f32_e32 v145, v157, v33
	v_cvt_pk_f16_f32 v18, v149, v237
	ds_write_b16 v158, v0 offset:3456
	ds_write_b16_d16_hi v158, v0 offset:8064
	ds_write_b16 v158, v3 offset:3600
	ds_write_b16_d16_hi v158, v3 offset:8208
	v_cvt_pk_f16_f32 v2, v238, v144
	v_cvt_f16_f32_e32 v4, v145
	ds_write_b16 v158, v18 offset:4752
	ds_write_b16_d16_hi v158, v18 offset:3744
	ds_write_b16 v158, v2 offset:8352
	ds_write_b16_d16_hi v158, v2 offset:3888
	ds_write_b16 v158, v4 offset:8496
	s_waitcnt lgkmcnt(0)
	s_barrier
	ds_read_b128 v[16:19], v159 offset:43520
	s_waitcnt lgkmcnt(0)
	v_mfma_f32_32x32x16_f16 v[32:47], v[16:19], v[126:129], 0
	ds_read_b128 v[2:5], v159 offset:34816
	v_mul_f32_e32 v0, v160, v160
	v_fmac_f32_e32 v0, v1, v1
	v_mul_f32_e32 v6, v162, v162
	v_add_f32_e32 v0, v0, v193
	v_add_f32_e32 v1, v161, v162
	v_fmac_f32_e32 v6, v161, v161
	s_waitcnt lgkmcnt(0)
	v_mfma_f32_32x32x16_f16 v[48:63], v[2:5], v[126:129], 0
	ds_read_b128 v[126:129], v159 offset:34848
	v_add_f32_e32 v1, v1, v196
	v_add_f32_e32 v0, v6, v0
	v_add_f32_e32 v6, v163, v164
	v_add_f32_e32 v1, v6, v1
	v_mul_f32_e32 v6, v164, v164
	v_fmac_f32_e32 v6, v163, v163
	v_add_f32_e32 v0, v6, v0
	v_add_f32_e32 v6, v165, v166
	v_add_f32_e32 v1, v6, v1
	v_mul_f32_e32 v6, v166, v166
	v_fmac_f32_e32 v6, v165, v165
	v_add_f32_e32 v20, v6, v0
	v_add_f32_e32 v0, v167, v168
	v_add_f32_e32 v21, v0, v1
	s_waitcnt lgkmcnt(0)
	v_mfma_f32_32x32x16_f16 v[48:63], v[126:129], v[118:121], v[48:63]
	v_mul_f32_e32 v22, v168, v168
	v_fmac_f32_e32 v22, v167, v167
	v_add_f32_e32 v160, v22, v20
	v_add_f32_e32 v20, v169, v170
	v_mul_f32_e32 v162, v170, v170
	v_add_f32_e32 v161, v20, v21
	v_fmac_f32_e32 v162, v169, v169
	v_mfma_f32_32x32x16_f16 v[0:15], v[2:5], v[122:125], 0
	v_mfma_f32_32x32x16_f16 v[0:15], v[126:129], v[114:117], v[0:15]
	v_mfma_f32_32x32x16_f16 v[16:31], v[16:19], v[122:125], 0
	v_add_f32_e32 v123, v171, v172
	v_add_f32_e32 v122, v162, v160
	v_add_f32_e32 v160, v123, v161
	v_mul_f32_e32 v123, v172, v172
	v_fmac_f32_e32 v123, v171, v171
	v_add_f32_e32 v161, v123, v122
	ds_read_b128 v[122:125], v159 offset:43552
	v_add_f32_e32 v162, v173, v174
	v_add_f32_e32 v160, v162, v160
	v_mul_f32_e32 v162, v174, v174
	v_fmac_f32_e32 v162, v173, v173
	s_waitcnt lgkmcnt(0)
	v_mfma_f32_32x32x16_f16 v[32:47], v[122:125], v[118:121], v[32:47]
	v_mul_f32_e32 v118, v176, v176
	v_add_f32_e32 v161, v162, v161
	v_add_f32_e32 v162, v175, v176
	v_fmac_f32_e32 v118, v175, v175
	v_mul_f32_e32 v120, v178, v178
	v_add_f32_e32 v160, v162, v160
	v_add_f32_e32 v118, v118, v161
	v_add_f32_e32 v119, v177, v178
	v_fmac_f32_e32 v120, v177, v177
	v_add_f32_e32 v119, v119, v160
	v_add_f32_e32 v118, v120, v118
	v_add_f32_e32 v120, v179, v180
	v_add_f32_e32 v126, v120, v119
	v_mul_f32_e32 v119, v180, v180
	v_mfma_f32_32x32x16_f16 v[16:31], v[122:125], v[114:117], v[16:31]
	v_add_f32_e32 v114, v181, v183
	v_fmac_f32_e32 v119, v179, v179
	v_add_f32_e32 v122, v114, v126
	v_mul_f32_e32 v114, v183, v183
	v_add_f32_e32 v127, v119, v118
	v_fmac_f32_e32 v114, v181, v181
	ds_read_b128 v[118:121], v159 offset:34880
	v_add_f32_e32 v123, v114, v127
	ds_read_b128 v[114:117], v159 offset:43584
	v_add_f32_e32 v124, v182, v184
	v_add_f32_e32 v122, v124, v122
	v_mul_f32_e32 v124, v184, v184
	v_fmac_f32_e32 v124, v182, v182
	s_waitcnt lgkmcnt(1)
	v_mfma_f32_32x32x16_f16 v[48:63], v[118:121], v[110:113], v[48:63]
	v_add_f32_e32 v123, v124, v123
	v_add_f32_e32 v124, v185, v186
	v_add_f32_e32 v124, 0, v124
	v_add_f32_e32 v122, 0, v122
	s_waitcnt lgkmcnt(0)
	v_mfma_f32_32x32x16_f16 v[32:47], v[114:117], v[110:113], v[32:47]
	v_mul_f32_e32 v110, v186, v186
	v_mul_f32_e32 v112, v188, v188
	v_fmac_f32_e32 v110, v185, v185
	v_add_f32_e32 v111, v187, v188
	v_fmac_f32_e32 v112, v187, v187
	v_add_f32_e32 v111, v111, v124
	v_add_f32_e32 v110, v110, v112
	v_add_f32_e32 v112, v189, v190
	v_mfma_f32_32x32x16_f16 v[0:15], v[118:121], v[106:109], v[0:15]
	v_add_f32_e32 v118, v112, v111
	v_mul_f32_e32 v111, v190, v190
	v_fmac_f32_e32 v111, v189, v189
	v_add_f32_e32 v119, v111, v110
	v_add_f32_e32 v120, v191, v192
	ds_read_b128 v[110:113], v159 offset:34912
	v_mfma_f32_32x32x16_f16 v[16:31], v[114:117], v[106:109], v[16:31]
	v_mul_f32_e32 v107, v192, v192
	v_fmac_f32_e32 v107, v191, v191
	v_add_f32_e32 v106, v120, v118
	v_add_f32_e32 v114, v107, v119
	v_add_f32_e32 v107, v194, v195
	v_add_f32_e32 v115, v107, v106
	ds_read_b128 v[106:109], v159 offset:43616
	v_mul_f32_e32 v116, v195, v195
	v_fmac_f32_e32 v116, v194, v194
	v_add_f32_e32 v114, v116, v114
	v_add_f32_e32 v116, v197, v199
	v_add_f32_e32 v115, v116, v115
	v_mul_f32_e32 v116, v199, v199
	s_waitcnt lgkmcnt(1)
	v_mfma_f32_32x32x16_f16 v[48:63], v[110:113], v[102:105], v[48:63]
	v_fmac_f32_e32 v116, v197, v197
	s_waitcnt lgkmcnt(0)
	v_mfma_f32_32x32x16_f16 v[32:47], v[106:109], v[102:105], v[32:47]
	v_mul_f32_e32 v104, v202, v202
	v_add_f32_e32 v102, v116, v114
	v_add_f32_e32 v103, v201, v202
	v_fmac_f32_e32 v104, v201, v201
	v_add_f32_e32 v103, v103, v115
	v_add_f32_e32 v102, v104, v102
	v_add_f32_e32 v104, v205, v206
	v_add_f32_e32 v103, v104, v103
	v_mul_f32_e32 v104, v206, v206
	v_mfma_f32_32x32x16_f16 v[0:15], v[110:113], v[98:101], v[0:15]
	v_fmac_f32_e32 v104, v205, v205
	v_add_f32_e32 v110, v104, v102
	v_add_f32_e32 v102, v207, v209
	v_add_f32_e32 v111, v102, v103
	ds_read_b128 v[102:105], v159 offset:34944
	v_mfma_f32_32x32x16_f16 v[16:31], v[106:109], v[98:101], v[16:31]
	v_mul_f32_e32 v98, v209, v209
	v_fmac_f32_e32 v98, v207, v207
	v_add_f32_e32 v106, v98, v110
	v_add_f32_e32 v98, v208, v210
	v_add_f32_e32 v107, v98, v111
	ds_read_b128 v[98:101], v159 offset:43648
	v_mul_f32_e32 v108, v210, v210
	v_fmac_f32_e32 v108, v208, v208
	v_add_f32_e32 v106, v108, v106
	v_add_f32_e32 v108, v211, v212
	s_waitcnt lgkmcnt(1)
	v_mfma_f32_32x32x16_f16 v[48:63], v[102:105], v[94:97], v[48:63]
	v_add_f32_e32 v107, v108, v107
	v_mul_f32_e32 v108, v212, v212
	v_fmac_f32_e32 v108, v211, v211
	v_add_f32_e32 v106, v108, v106
	s_waitcnt lgkmcnt(0)
	v_mfma_f32_32x32x16_f16 v[32:47], v[98:101], v[94:97], v[32:47]
	v_add_f32_e32 v94, v213, v214
	v_add_f32_e32 v94, v94, v107
	v_mul_f32_e32 v95, v214, v214
	v_add_f32_e32 v96, v215, v216
	v_fmac_f32_e32 v95, v213, v213
	v_add_f32_e32 v94, v96, v94
	v_mul_f32_e32 v96, v216, v216
	v_add_f32_e32 v95, v95, v106
	v_fmac_f32_e32 v96, v215, v215
	v_mfma_f32_32x32x16_f16 v[0:15], v[102:105], v[86:89], v[0:15]
	v_add_f32_e32 v102, v96, v95
	v_add_f32_e32 v95, v217, v218
	v_add_f32_e32 v103, v95, v94
	ds_read_b128 v[94:97], v159 offset:34976
	v_mul_f32_e32 v104, v218, v218
	v_fmac_f32_e32 v104, v217, v217
	v_mfma_f32_32x32x16_f16 v[16:31], v[98:101], v[86:89], v[16:31]
	v_add_f32_e32 v86, v219, v221
	v_add_f32_e32 v99, v86, v103
	ds_read_b128 v[86:89], v159 offset:43680
	v_mul_f32_e32 v100, v221, v221
	v_add_f32_e32 v98, v104, v102
	v_fmac_f32_e32 v100, v219, v219
	v_add_f32_e32 v98, v100, v98
	s_waitcnt lgkmcnt(1)
	v_mfma_f32_32x32x16_f16 v[48:63], v[94:97], v[90:93], v[48:63]
	v_add_f32_e32 v100, v220, v222
	v_add_f32_e32 v99, v100, v99
	v_mul_f32_e32 v100, v222, v222
	v_fmac_f32_e32 v100, v220, v220
	v_add_f32_e32 v98, v100, v98
	v_add_f32_e32 v98, v123, v98
	v_add_f32_e32 v99, v122, v99
	s_waitcnt lgkmcnt(0)
	v_mfma_f32_32x32x16_f16 v[32:47], v[86:89], v[90:93], v[32:47]
	v_add_f32_e32 v90, v146, v147
	v_add_f32_e32 v90, 0, v90
	v_add_f32_e32 v92, v148, v149
	v_mul_f32_e32 v91, v147, v147
	v_add_f32_e32 v90, v92, v90
	v_mul_f32_e32 v92, v149, v149
	v_fmac_f32_e32 v91, v146, v146
	v_fmac_f32_e32 v92, v148, v148
	v_mfma_f32_32x32x16_f16 v[0:15], v[94:97], v[78:81], v[0:15]
	v_add_f32_e32 v94, v91, v92
	v_add_f32_e32 v91, v150, v151
	v_add_f32_e32 v95, v91, v90
	ds_read_b128 v[90:93], v159 offset:35008
	v_mul_f32_e32 v96, v151, v151
	v_fmac_f32_e32 v96, v150, v150
	v_mfma_f32_32x32x16_f16 v[16:31], v[86:89], v[78:81], v[16:31]
	v_add_f32_e32 v78, v152, v153
	v_add_f32_e32 v87, v78, v95
	ds_read_b128 v[78:81], v159 offset:43712
	v_mul_f32_e32 v88, v153, v153
	v_add_f32_e32 v86, v96, v94
	v_fmac_f32_e32 v88, v152, v152
	v_add_f32_e32 v86, v88, v86
	v_add_f32_e32 v88, v154, v155
	v_add_f32_e32 v87, v88, v87
	v_mul_f32_e32 v88, v155, v155
	v_fmac_f32_e32 v88, v154, v154
	v_add_f32_e32 v86, v88, v86
	v_add_f32_e32 v88, v198, v200
	s_waitcnt lgkmcnt(1)
	v_mfma_f32_32x32x16_f16 v[48:63], v[90:93], v[82:85], v[48:63]
	s_waitcnt lgkmcnt(0)
	v_mfma_f32_32x32x16_f16 v[32:47], v[78:81], v[82:85], v[32:47]
	v_add_f32_e32 v82, v88, v87
	v_mul_f32_e32 v83, v200, v200
	v_add_f32_e32 v84, v203, v204
	v_fmac_f32_e32 v83, v198, v198
	v_add_f32_e32 v82, v84, v82
	v_mul_f32_e32 v84, v204, v204
	v_add_f32_e32 v83, v83, v86
	v_fmac_f32_e32 v84, v203, v203
	v_add_f32_e32 v86, v84, v83
	v_add_f32_e32 v83, v223, v224
	v_mfma_f32_32x32x16_f16 v[0:15], v[90:93], v[70:73], v[0:15]
	v_add_f32_e32 v87, v83, v82
	v_mul_f32_e32 v88, v224, v224
	v_fmac_f32_e32 v88, v223, v223
	ds_read_b128 v[82:85], v159 offset:35040
	v_mfma_f32_32x32x16_f16 v[16:31], v[78:81], v[70:73], v[16:31]
	v_add_f32_e32 v71, v225, v226
	v_add_f32_e32 v78, v71, v87
	v_mul_f32_e32 v71, v226, v226
	v_add_f32_e32 v70, v88, v86
	v_fmac_f32_e32 v71, v225, v225
	v_add_f32_e32 v79, v71, v70
	ds_read_b128 v[70:73], v159 offset:43744
	s_waitcnt lgkmcnt(1)
	v_mfma_f32_32x32x16_f16 v[48:63], v[82:85], v[74:77], v[48:63]
	v_add_f32_e32 v80, v227, v228
	v_add_f32_e32 v78, v80, v78
	v_mul_f32_e32 v80, v228, v228
	v_fmac_f32_e32 v80, v227, v227
	v_add_f32_e32 v79, v80, v79
	v_add_f32_e32 v80, v229, v230
	v_add_f32_e32 v78, v80, v78
	v_mfma_f32_32x32x16_f16 v[0:15], v[82:85], v[66:69], v[0:15]
	s_nop 3
	v_cvt_pk_f16_f32 v55, v54, v55
	v_cvt_pk_f16_f32 v54, v52, v53
	v_cvt_pk_f16_f32 v53, v50, v51
	v_cvt_pk_f16_f32 v52, v48, v49
	s_waitcnt vmcnt(3)
	s_waitcnt lgkmcnt(0)
	v_mfma_f32_32x32x16_f16 v[16:31], v[70:73], v[66:69], v[16:31]
	v_lshrrev_b32_e32 v69, 16, v139
	v_mfma_f32_32x32x16_f16 v[32:47], v[70:73], v[74:77], v[32:47]
	v_lshrrev_b32_e32 v70, 8, v139
	v_perm_b32 v69, v70, v69, s2
	v_perm_b32 v66, v240, v138, s42
	v_perm_b32 v67, v240, v138, s43
	v_perm_b32 v68, v240, v139, s42
	v_or_b32_e32 v69, 0x64006400, v69
	v_pk_add_f16 v66, v66, s3 op_sel_hi:[1,0]
	v_pk_add_f16 v67, v67, s3 op_sel_hi:[1,0]
	v_pk_add_f16 v68, v68, s3 op_sel_hi:[1,0]
	v_pk_add_f16 v69, v69, s3 op_sel_hi:[1,0]
	s_nop 1
	v_mfma_f32_32x32x16_f16 v[0:15], v[66:69], v[52:55], v[0:15]
	v_perm_b32 v48, v240, v136, s42
	v_perm_b32 v49, v240, v136, s43
	v_perm_b32 v50, v240, v137, s42
	v_perm_b32 v51, v240, v137, s43
	v_pk_add_f16 v48, v48, s3 op_sel_hi:[1,0]
	v_pk_add_f16 v49, v49, s3 op_sel_hi:[1,0]
	v_pk_add_f16 v50, v50, s3 op_sel_hi:[1,0]
	v_pk_add_f16 v51, v51, s3 op_sel_hi:[1,0]
	v_cvt_pk_f16_f32 v39, v38, v39
	v_cvt_pk_f16_f32 v38, v36, v37
	v_mfma_f32_32x32x16_f16 v[16:31], v[48:51], v[52:55], v[16:31]
	v_perm_b32 v48, v240, v134, s42
	v_perm_b32 v49, v240, v134, s43
	v_perm_b32 v50, v240, v135, s42
	v_perm_b32 v51, v240, v135, s43
	v_pk_add_f16 v48, v48, s3 op_sel_hi:[1,0]
	v_pk_add_f16 v49, v49, s3 op_sel_hi:[1,0]
	v_pk_add_f16 v50, v50, s3 op_sel_hi:[1,0]
	v_pk_add_f16 v51, v51, s3 op_sel_hi:[1,0]
	v_cvt_pk_f16_f32 v55, v62, v63
	v_cvt_pk_f16_f32 v54, v60, v61
	v_cvt_pk_f16_f32 v53, v58, v59
	v_cvt_pk_f16_f32 v52, v56, v57
	s_waitcnt vmcnt(2)
	v_cvt_pk_f16_f32 v37, v34, v35
	v_mfma_f32_32x32x16_f16 v[0:15], v[48:51], v[52:55], v[0:15]
	v_perm_b32 v48, v240, v142, s42
	v_perm_b32 v49, v240, v142, s43
	v_perm_b32 v50, v240, v143, s42
	v_perm_b32 v51, v240, v143, s43
	v_pk_add_f16 v48, v48, s3 op_sel_hi:[1,0]
	v_pk_add_f16 v49, v49, s3 op_sel_hi:[1,0]
	v_pk_add_f16 v50, v50, s3 op_sel_hi:[1,0]
	v_pk_add_f16 v51, v51, s3 op_sel_hi:[1,0]
	v_cvt_pk_f16_f32 v36, v32, v33
	s_waitcnt vmcnt(1)
	v_mfma_f32_32x32x16_f16 v[16:31], v[48:51], v[52:55], v[16:31]
	v_lshrrev_b32_e32 v51, 16, v133
	v_lshrrev_b32_e32 v52, 8, v133
	v_perm_b32 v51, v52, v51, s2
	v_perm_b32 v48, v240, v132, s42
	v_perm_b32 v49, v240, v132, s43
	v_perm_b32 v50, v240, v133, s42
	v_or_b32_e32 v51, 0x64006400, v51
	v_pk_add_f16 v48, v48, s3 op_sel_hi:[1,0]
	v_pk_add_f16 v49, v49, s3 op_sel_hi:[1,0]
	v_pk_add_f16 v50, v50, s3 op_sel_hi:[1,0]
	v_pk_add_f16 v51, v51, s3 op_sel_hi:[1,0]
	s_nop 1
	v_mfma_f32_32x32x16_f16 v[0:15], v[48:51], v[36:39], v[0:15]
	v_perm_b32 v32, v240, v140, s42
	v_perm_b32 v33, v240, v140, s43
	v_perm_b32 v34, v240, v141, s42
	v_perm_b32 v35, v240, v141, s43
	v_pk_add_f16 v32, v32, s3 op_sel_hi:[1,0]
	v_pk_add_f16 v33, v33, s3 op_sel_hi:[1,0]
	v_pk_add_f16 v34, v34, s3 op_sel_hi:[1,0]
	v_pk_add_f16 v35, v35, s3 op_sel_hi:[1,0]
	v_mul_f32_e32 v74, v230, v230
	v_fmac_f32_e32 v74, v229, v229
	v_mfma_f32_32x32x16_f16 v[16:31], v[32:35], v[36:39], v[16:31]
	v_perm_b32 v32, v240, v130, s42
	v_perm_b32 v33, v240, v130, s43
	v_perm_b32 v34, v240, v131, s42
	v_perm_b32 v35, v240, v131, s43
	v_pk_add_f16 v32, v32, s3 op_sel_hi:[1,0]
	v_pk_add_f16 v33, v33, s3 op_sel_hi:[1,0]
	v_pk_add_f16 v34, v34, s3 op_sel_hi:[1,0]
	v_pk_add_f16 v35, v35, s3 op_sel_hi:[1,0]
	v_cvt_pk_f16_f32 v39, v46, v47
	v_cvt_pk_f16_f32 v38, v44, v45
	v_cvt_pk_f16_f32 v37, v42, v43
	v_cvt_pk_f16_f32 v36, v40, v41
	s_waitcnt vmcnt(0)
	v_mul_f32_e32 v76, v232, v232
	v_mfma_f32_32x32x16_f16 v[0:15], v[32:35], v[36:39], v[0:15]
	v_perm_b32 v32, v240, v64, s42
	v_perm_b32 v33, v240, v64, s43
	v_perm_b32 v34, v240, v65, s42
	v_perm_b32 v35, v240, v65, s43
	v_pk_add_f16 v32, v32, s3 op_sel_hi:[1,0]
	v_pk_add_f16 v33, v33, s3 op_sel_hi:[1,0]
	v_pk_add_f16 v34, v34, s3 op_sel_hi:[1,0]
	v_pk_add_f16 v35, v35, s3 op_sel_hi:[1,0]
	s_nop 3
	v_add_f32_e32 v0, v157, v0
	v_add_f32_e32 v74, v74, v79
	v_mfma_f32_32x32x16_f16 v[16:31], v[32:35], v[36:39], v[16:31]
	v_cvt_f16_f32_e32 v33, v0
	v_add_f32_e32 v75, v231, v232
	v_fmac_f32_e32 v76, v231, v231
	v_add_f32_e32 v75, v75, v78
	ds_write_b16 v158, v33 offset:18432
	v_add_f32_e32 v74, v76, v74
	v_add_f32_e32 v76, v233, v234
	s_nop 4
	v_add_f32_e32 v16, v157, v16
	v_add_f32_e32 v32, v0, v16
	v_cvt_f16_f32_e32 v34, v16
	v_mul_f32_e32 v16, v16, v16
	v_fmac_f32_e32 v16, v0, v0
	v_add_f32_e32 v0, v157, v1
	v_add_f32_e32 v1, v157, v17
	v_add_f32_e32 v32, 0, v32
	v_add_f32_e32 v17, v0, v1
	v_add_f32_e32 v17, v17, v32
	v_mul_f32_e32 v32, v1, v1
	v_cvt_f16_f32_e32 v1, v1
	v_fmac_f32_e32 v32, v0, v0
	v_cvt_f16_f32_e32 v33, v0
	v_add_f32_e32 v0, v16, v32
	ds_write_b16 v158, v1 offset:23184
	v_add_f32_e32 v1, v157, v2
	v_add_f32_e32 v2, v157, v18
	v_add_f32_e32 v16, v1, v2
	v_add_f32_e32 v16, v16, v17
	v_mul_f32_e32 v17, v2, v2
	v_cvt_f16_f32_e32 v2, v2
	v_cvt_f16_f32_e32 v18, v1
	v_fmac_f32_e32 v17, v1, v1
	v_add_f32_e32 v1, v157, v3
	ds_write_b16 v158, v2 offset:23328
	v_add_f32_e32 v2, v157, v19
	v_add_f32_e32 v3, v1, v2
	v_add_f32_e32 v3, v3, v16
	v_mul_f32_e32 v16, v2, v2
	v_cvt_f16_f32_e32 v2, v2
	v_add_f32_e32 v0, v17, v0
	v_cvt_f16_f32_e32 v17, v1
	v_fmac_f32_e32 v16, v1, v1
	ds_write_b16 v158, v2 offset:23472
	v_add_f32_e32 v1, v157, v4
	v_add_f32_e32 v2, v157, v20
	v_add_f32_e32 v4, v1, v2
	v_add_f32_e32 v3, v4, v3
	v_mul_f32_e32 v4, v2, v2
	v_cvt_f16_f32_e32 v2, v2
	v_add_f32_e32 v0, v16, v0
	v_cvt_f16_f32_e32 v16, v1
	v_fmac_f32_e32 v4, v1, v1
	ds_write_b16 v158, v2 offset:24192
	v_add_f32_e32 v1, v157, v5
	v_add_f32_e32 v2, v157, v21
	v_add_f32_e32 v0, v4, v0
	v_add_f32_e32 v4, v1, v2
	v_add_f32_e32 v3, v4, v3
	v_mul_f32_e32 v4, v2, v2
	v_cvt_f16_f32_e32 v2, v2
	v_cvt_f16_f32_e32 v5, v1
	v_fmac_f32_e32 v4, v1, v1
	v_add_f32_e32 v1, v157, v6
	ds_write_b16 v158, v2 offset:24336
	v_add_f32_e32 v2, v157, v22
	v_add_f32_e32 v0, v4, v0
	v_add_f32_e32 v4, v1, v2
	v_add_f32_e32 v3, v4, v3
	v_mul_f32_e32 v4, v2, v2
	v_cvt_f16_f32_e32 v2, v2
	ds_write_b16 v158, v5 offset:19728
	v_cvt_f16_f32_e32 v5, v1
	v_fmac_f32_e32 v4, v1, v1
	ds_write_b16 v158, v2 offset:24480
	v_add_f32_e32 v1, v157, v7
	v_add_f32_e32 v2, v157, v23
	v_add_f32_e32 v0, v4, v0
	v_add_f32_e32 v4, v1, v2
	v_add_f32_e32 v3, v4, v3
	v_mul_f32_e32 v4, v2, v2
	v_cvt_f16_f32_e32 v2, v2
	ds_write_b16 v158, v5 offset:19872
	v_cvt_f16_f32_e32 v5, v1
	v_fmac_f32_e32 v4, v1, v1
	ds_write_b16 v158, v2 offset:24624
	v_add_f32_e32 v1, v157, v8
	v_add_f32_e32 v2, v157, v24
	v_add_f32_e32 v0, v4, v0
	v_add_f32_e32 v4, v1, v2
	v_add_f32_e32 v3, v4, v3
	v_mul_f32_e32 v4, v2, v2
	v_cvt_f16_f32_e32 v2, v2
	ds_write_b16 v158, v5 offset:20016
	v_cvt_f16_f32_e32 v5, v1
	v_fmac_f32_e32 v4, v1, v1
	ds_write_b16 v158, v2 offset:25344
	v_add_f32_e32 v1, v157, v9
	v_add_f32_e32 v2, v157, v25
	v_add_f32_e32 v0, v4, v0
	v_add_f32_e32 v4, v1, v2
	v_add_f32_e32 v3, v4, v3
	v_mul_f32_e32 v4, v2, v2
	v_cvt_f16_f32_e32 v2, v2
	ds_write_b16 v158, v5 offset:20736
	v_cvt_f16_f32_e32 v5, v1
	v_fmac_f32_e32 v4, v1, v1
	ds_write_b16 v158, v2 offset:25488
	v_add_f32_e32 v1, v157, v10
	v_add_f32_e32 v2, v157, v26
	v_add_f32_e32 v0, v4, v0
	v_add_f32_e32 v4, v1, v2
	v_add_f32_e32 v3, v4, v3
	v_mul_f32_e32 v4, v2, v2
	v_cvt_f16_f32_e32 v2, v2
	ds_write_b16 v158, v5 offset:20880
	v_cvt_f16_f32_e32 v5, v1
	v_fmac_f32_e32 v4, v1, v1
	ds_write_b16 v158, v2 offset:25632
	v_add_f32_e32 v1, v157, v11
	v_add_f32_e32 v2, v157, v27
	v_add_f32_e32 v0, v4, v0
	v_add_f32_e32 v4, v1, v2
	v_add_f32_e32 v3, v4, v3
	v_mul_f32_e32 v4, v2, v2
	v_cvt_f16_f32_e32 v2, v2
	ds_write_b16 v158, v5 offset:21024
	v_cvt_f16_f32_e32 v5, v1
	v_fmac_f32_e32 v4, v1, v1
	ds_write_b16 v158, v2 offset:25776
	v_add_f32_e32 v1, v157, v12
	v_add_f32_e32 v2, v157, v28
	v_add_f32_e32 v0, v4, v0
	v_add_f32_e32 v4, v1, v2
	v_add_f32_e32 v3, v4, v3
	v_mul_f32_e32 v4, v2, v2
	v_cvt_f16_f32_e32 v2, v2
	ds_write_b16 v158, v5 offset:21168
	v_cvt_f16_f32_e32 v5, v1
	v_fmac_f32_e32 v4, v1, v1
	ds_write_b16 v158, v2 offset:26496
	v_add_f32_e32 v1, v157, v13
	v_add_f32_e32 v2, v157, v29
	v_add_f32_e32 v0, v4, v0
	v_add_f32_e32 v4, v1, v2
	v_add_f32_e32 v3, v4, v3
	v_mul_f32_e32 v4, v2, v2
	v_cvt_f16_f32_e32 v2, v2
	ds_write_b16 v158, v5 offset:21888
	v_cvt_f16_f32_e32 v5, v1
	v_fmac_f32_e32 v4, v1, v1
	ds_write_b16 v158, v2 offset:26640
	v_add_f32_e32 v1, v157, v14
	v_add_f32_e32 v2, v157, v30
	v_add_f32_e32 v0, v4, v0
	v_add_f32_e32 v4, v1, v2
	v_add_f32_e32 v3, v4, v3
	v_cvt_f16_f32_e32 v4, v1
	v_add_f32_e32 v75, v76, v75
	v_mul_f32_e32 v76, v234, v234
	ds_write_b16 v158, v5 offset:22032
	v_mul_f32_e32 v5, v2, v2
	v_fmac_f32_e32 v76, v233, v233
	v_mul_f32_e32 v67, v236, v236
	v_fmac_f32_e32 v5, v1, v1
	v_add_f32_e32 v74, v76, v74
	v_fmac_f32_e32 v67, v235, v235
	v_mul_f32_e32 v57, v238, v238
	v_add_f32_e32 v0, v5, v0
	v_cvt_f16_f32_e32 v5, v2
	v_add_f32_e32 v1, v157, v15
	v_add_f32_e32 v2, v157, v31
	v_add_f32_e32 v76, v235, v236
	v_add_f32_e32 v67, v67, v74
	v_fmac_f32_e32 v57, v237, v237
	v_mul_f32_e32 v50, v145, v145
	ds_write_b16 v158, v4 offset:22176
	v_add_f32_e32 v4, v1, v2
	v_add_f32_e32 v66, v76, v75
	v_add_f32_e32 v56, v237, v238
	v_add_f32_e32 v48, v57, v67
	v_fmac_f32_e32 v50, v144, v144
	v_add_f32_e32 v3, v4, v3
	v_mul_f32_e32 v4, v2, v2
	v_add_f32_e32 v56, v56, v66
	v_add_f32_e32 v49, v144, v145
	v_add_f32_e32 v40, v50, v48
	v_fmac_f32_e32 v4, v1, v1
	v_add_f32_e32 v49, v49, v56
	v_add_f32_e32 v40, v98, v40
	v_add_f32_e32 v4, v4, v0
	v_add_f32_e32 v41, v99, v49
	v_cvt_pk_f16_f32 v6, v1, v2
	v_add_f32_e32 v1, v40, v4
	v_lshlrev_b32_e32 v4, 2, v156
	v_add_f32_e32 v0, v41, v3
	v_xor_b32_e32 v3, 0x80, v4
	s_nop 0
	ds_bpermute_b32 v2, v3, v0
	ds_bpermute_b32 v3, v3, v1
	ds_write_b16 v158, v34 offset:23040
	ds_write_b16 v158, v33 offset:18576
	ds_write_b16 v158, v18 offset:18720
	ds_write_b16 v158, v17 offset:18864
	ds_write_b16 v158, v16 offset:19584
	ds_write_b16 v158, v5 offset:26784
	ds_write_b16 v158, v6 offset:22320
	ds_write_b16_d16_hi v158, v6 offset:26928
	s_and_saveexec_b64 s[0:1], vcc
	s_cbranch_execz .LBB3_26
	s_lshl_b32 s2, s13, 5
	v_lshl_add_u32 v4, s2, 2, v4
	v_or_b32_e32 v5, 0x1e400, v4
	s_waitcnt lgkmcnt(9)
	v_add_f32_e32 v0, v0, v2
	v_add_u32_e32 v4, 0x1e500, v4
	s_waitcnt lgkmcnt(8)
	v_add_f32_e32 v1, v1, v3
	ds_add_f32 v5, v0
	ds_add_f32 v4, v1

	.amdhsa_kernel _Z7k_layerILi0EEvPKDF16_S1_PKfS3_S3_S3_S3_S3_S1_S1_S1_S1_S3_S3_PKhS5_PDF16_S6_PfS7_
		.amdhsa_group_segment_fixed_size 126720
		.amdhsa_private_segment_fixed_size 0
		.amdhsa_kernarg_size 160
		.amdhsa_user_sgpr_count 2
		.amdhsa_user_sgpr_dispatch_ptr 0
		.amdhsa_user_sgpr_queue_ptr 0
		.amdhsa_user_sgpr_kernarg_segment_ptr 1
		.amdhsa_user_sgpr_dispatch_id 0
		.amdhsa_user_sgpr_kernarg_preload_length 0
		.amdhsa_user_sgpr_kernarg_preload_offset 0
		.amdhsa_user_sgpr_private_segment_size 0
		.amdhsa_uses_dynamic_stack 0
		.amdhsa_enable_private_segment 0
		.amdhsa_system_sgpr_workgroup_id_x 1
		.amdhsa_system_sgpr_workgroup_id_y 0
		.amdhsa_system_sgpr_workgroup_id_z 0
		.amdhsa_system_sgpr_workgroup_info 0
		.amdhsa_system_vgpr_workitem_id 0
		.amdhsa_next_free_vgpr 256
		.amdhsa_next_free_sgpr 96
		.amdhsa_accum_offset 256
		.amdhsa_reserve_vcc 1
		.amdhsa_float_round_mode_32 0
		.amdhsa_float_round_mode_16_64 0
		.amdhsa_float_denorm_mode_32 3
		.amdhsa_float_denorm_mode_16_64 3
		.amdhsa_dx10_clamp 1
		.amdhsa_ieee_mode 1
		.amdhsa_fp16_overflow 0
		.amdhsa_tg_split 0
		.amdhsa_exception_fp_ieee_invalid_op 0
		.amdhsa_exception_fp_denorm_src 0
		.amdhsa_exception_fp_ieee_div_zero 0
		.amdhsa_exception_fp_ieee_overflow 0
		.amdhsa_exception_fp_ieee_underflow 0
		.amdhsa_exception_fp_ieee_inexact 0
		.amdhsa_exception_int_div_zero 0
	.end_amdhsa_kernel

amdhsa.kernels:
  - .agpr_count:     32
    .args:
      - .actual_access:  read_only
        .address_space:  global
        .offset:         0
        .size:           8
        .value_kind:     global_buffer
      - .actual_access:  read_only
        .address_space:  global
        .offset:         8
        .size:           8
        .value_kind:     global_buffer
      - .actual_access:  read_only
        .address_space:  global
        .offset:         16
        .size:           8
        .value_kind:     global_buffer
      - .actual_access:  write_only
        .address_space:  global
        .offset:         24
        .size:           8
        .value_kind:     global_buffer
      - .actual_access:  read_only
        .address_space:  global
        .offset:         32
        .size:           8
        .value_kind:     global_buffer
      - .actual_access:  read_only
        .address_space:  global
        .offset:         40
        .size:           8
        .value_kind:     global_buffer
      - .actual_access:  read_only
        .address_space:  global
        .offset:         48
        .size:           8
        .value_kind:     global_buffer
      - .actual_access:  read_only
        .address_space:  global
        .offset:         56
        .size:           8
        .value_kind:     global_buffer
      - .actual_access:  read_only
        .address_space:  global
        .offset:         64
        .size:           8
        .value_kind:     global_buffer
      - .actual_access:  read_only
        .address_space:  global
        .offset:         72
        .size:           8
        .value_kind:     global_buffer
      - .actual_access:  read_only
        .address_space:  global
        .offset:         80
        .size:           8
        .value_kind:     global_buffer
      - .actual_access:  write_only
        .address_space:  global
        .offset:         88
        .size:           8
        .value_kind:     global_buffer
      - .actual_access:  write_only
        .address_space:  global
        .offset:         96
        .size:           8
        .value_kind:     global_buffer
      - .actual_access:  write_only
        .address_space:  global
        .offset:         104
        .size:           8
        .value_kind:     global_buffer
      - .actual_access:  write_only
        .address_space:  global
        .offset:         112
        .size:           8
        .value_kind:     global_buffer
      - .actual_access:  write_only
        .address_space:  global
        .offset:         120
        .size:           8
        .value_kind:     global_buffer
    .group_segment_fixed_size: 17408
    .kernarg_segment_align: 8
    .kernarg_segment_size: 128
    .language:       OpenCL C
    .language_version:
      - 2
      - 0
    .max_flat_workgroup_size: 256
    .name:           _Z9k_encprepPKfS0_S0_PDF16_PKiS3_S0_S0_S0_S0_S0_PhS4_S1_S1_Pf
    .private_segment_fixed_size: 0
    .sgpr_count:     22
    .sgpr_spill_count: 0
    .symbol:         _Z9k_encprepPKfS0_S0_PDF16_PKiS3_S0_S0_S0_S0_S0_PhS4_S1_S1_Pf.kd
    .uniform_work_group_size: 1
    .uses_dynamic_stack: false
    .vgpr_count:     128
    .vgpr_spill_count: 0
    .wavefront_size: 64
  - .agpr_count:     0
    .args:
      - .actual_access:  read_only
        .address_space:  global
        .offset:         0
        .size:           8
        .value_kind:     global_buffer
      - .actual_access:  read_only
        .address_space:  global
        .offset:         8
        .size:           8
        .value_kind:     global_buffer
      - .actual_access:  read_only
        .address_space:  global
        .offset:         16
        .size:           8
        .value_kind:     global_buffer
      - .actual_access:  read_only
        .address_space:  global
        .offset:         24
        .size:           8
        .value_kind:     global_buffer
      - .actual_access:  read_only
        .address_space:  global
        .offset:         32
        .size:           8
        .value_kind:     global_buffer
      - .actual_access:  read_only
        .address_space:  global
        .offset:         40
        .size:           8
        .value_kind:     global_buffer
      - .actual_access:  read_only
        .address_space:  global
        .offset:         48
        .size:           8
        .value_kind:     global_buffer
      - .actual_access:  read_only
        .address_space:  global
        .offset:         56
        .size:           8
        .value_kind:     global_buffer
      - .actual_access:  read_only
        .address_space:  global
        .offset:         64
        .size:           8
        .value_kind:     global_buffer
      - .actual_access:  read_only
        .address_space:  global
        .offset:         72
        .size:           8
        .value_kind:     global_buffer
      - .actual_access:  read_only
        .address_space:  global
        .offset:         80
        .size:           8
        .value_kind:     global_buffer
      - .actual_access:  read_only
        .address_space:  global
        .offset:         88
        .size:           8
        .value_kind:     global_buffer
      - .actual_access:  write_only
        .address_space:  global
        .offset:         96
        .size:           8
        .value_kind:     global_buffer
    .group_segment_fixed_size: 40448
    .kernarg_segment_align: 8
    .kernarg_segment_size: 104
    .language:       OpenCL C
    .language_version:
      - 2
      - 0
    .max_flat_workgroup_size: 1024
    .name:           _Z7k_finalPKDF16_S0_PKfS2_S2_S2_S2_S2_S0_S2_S2_S2_Pf
    .private_segment_fixed_size: 0
    .sgpr_count:     24
    .sgpr_spill_count: 0
    .symbol:         _Z7k_finalPKDF16_S0_PKfS2_S2_S2_S2_S2_S0_S2_S2_S2_Pf.kd
    .uniform_work_group_size: 1
    .uses_dynamic_stack: false
    .vgpr_count:     99
    .vgpr_spill_count: 0
    .wavefront_size: 64
  - .agpr_count:     0
    .args:
      - .actual_access:  read_only
        .address_space:  global
        .offset:         0
        .size:           8
        .value_kind:     global_buffer
      - .actual_access:  read_only
        .address_space:  global
        .offset:         8
        .size:           8
        .value_kind:     global_buffer
      - .actual_access:  read_only
        .address_space:  global
        .offset:         16
        .size:           8
        .value_kind:     global_buffer
      - .actual_access:  read_only
        .address_space:  global
        .offset:         24
        .size:           8
        .value_kind:     global_buffer
      - .actual_access:  read_only
        .address_space:  global
        .offset:         32
        .size:           8
        .value_kind:     global_buffer
      - .actual_access:  read_only
        .address_space:  global
        .offset:         40
        .size:           8
        .value_kind:     global_buffer
      - .actual_access:  read_only
        .address_space:  global
        .offset:         48
        .size:           8
        .value_kind:     global_buffer
      - .actual_access:  read_only
        .address_space:  global
        .offset:         56
        .size:           8
        .value_kind:     global_buffer
      - .actual_access:  read_only
        .address_space:  global
        .offset:         64
        .size:           8
        .value_kind:     global_buffer
      - .actual_access:  read_only
        .address_space:  global
        .offset:         72
        .size:           8
        .value_kind:     global_buffer
      - .actual_access:  read_only
        .address_space:  global
        .offset:         80
        .size:           8
        .value_kind:     global_buffer
      - .actual_access:  read_only
        .address_space:  global
        .offset:         88
        .size:           8
        .value_kind:     global_buffer
      - .actual_access:  read_only
        .address_space:  global
        .offset:         96
        .size:           8
        .value_kind:     global_buffer
      - .actual_access:  read_only
        .address_space:  global
        .offset:         104
        .size:           8
        .value_kind:     global_buffer
      - .actual_access:  read_only
        .address_space:  global
        .offset:         112
        .size:           8
        .value_kind:     global_buffer
      - .actual_access:  read_only
        .address_space:  global
        .offset:         120
        .size:           8
        .value_kind:     global_buffer
      - .actual_access:  write_only
        .address_space:  global
        .offset:         128
        .size:           8
        .value_kind:     global_buffer
      - .actual_access:  write_only
        .address_space:  global
        .offset:         136
        .size:           8
        .value_kind:     global_buffer
      - .address_space:  global
        .offset:         144
        .size:           8
        .value_kind:     global_buffer
      - .address_space:  global
        .offset:         152
        .size:           8
        .value_kind:     global_buffer
    .group_segment_fixed_size: 126720
    .kernarg_segment_align: 8
    .kernarg_segment_size: 160
    .language:       OpenCL C
    .language_version:
      - 2
      - 0
    .max_flat_workgroup_size: 512
    .name:           _Z7k_layerILi1EEvPKDF16_S1_PKfS3_S3_S3_S3_S3_S1_S1_S1_S1_S3_S3_PKhS5_PDF16_S6_PfS7_
    .private_segment_fixed_size: 0
    .sgpr_count:     50
    .sgpr_spill_count: 0
    .symbol:         _Z7k_layerILi1EEvPKDF16_S1_PKfS3_S3_S3_S3_S3_S1_S1_S1_S1_S3_S3_PKhS5_PDF16_S6_PfS7_.kd
    .uniform_work_group_size: 1
    .uses_dynamic_stack: false
    .vgpr_count:     256
    .vgpr_spill_count: 0
    .wavefront_size: 64
  - .agpr_count:     0
    .args:
      - .actual_access:  read_only
        .address_space:  global
        .offset:         0
        .size:           8
        .value_kind:     global_buffer
      - .actual_access:  read_only
        .address_space:  global
        .offset:         8
        .size:           8
        .value_kind:     global_buffer
      - .actual_access:  read_only
        .address_space:  global
        .offset:         16
        .size:           8
        .value_kind:     global_buffer
      - .actual_access:  read_only
        .address_space:  global
        .offset:         24
        .size:           8
        .value_kind:     global_buffer
      - .actual_access:  read_only
        .address_space:  global
        .offset:         32
        .size:           8
        .value_kind:     global_buffer
      - .actual_access:  read_only
        .address_space:  global
        .offset:         40
        .size:           8
        .value_kind:     global_buffer
      - .actual_access:  read_only
        .address_space:  global
        .offset:         48
        .size:           8
        .value_kind:     global_buffer
      - .actual_access:  read_only
        .address_space:  global
        .offset:         56
        .size:           8
        .value_kind:     global_buffer
      - .actual_access:  read_only
        .address_space:  global
        .offset:         64
        .size:           8
        .value_kind:     global_buffer
      - .actual_access:  read_only
        .address_space:  global
        .offset:         72
        .size:           8
        .value_kind:     global_buffer
      - .actual_access:  read_only
        .address_space:  global
        .offset:         80
        .size:           8
        .value_kind:     global_buffer
      - .actual_access:  read_only
        .address_space:  global
        .offset:         88
        .size:           8
        .value_kind:     global_buffer
      - .actual_access:  read_only
        .address_space:  global
        .offset:         96
        .size:           8
        .value_kind:     global_buffer
      - .actual_access:  read_only
        .address_space:  global
        .offset:         104
        .size:           8
        .value_kind:     global_buffer
      - .actual_access:  read_only
        .address_space:  global
        .offset:         112
        .size:           8
        .value_kind:     global_buffer
      - .actual_access:  read_only
        .address_space:  global
        .offset:         120
        .size:           8
        .value_kind:     global_buffer
      - .actual_access:  write_only
        .address_space:  global
        .offset:         128
        .size:           8
        .value_kind:     global_buffer
      - .actual_access:  write_only
        .address_space:  global
        .offset:         136
        .size:           8
        .value_kind:     global_buffer
      - .address_space:  global
        .offset:         144
        .size:           8
        .value_kind:     global_buffer
      - .address_space:  global
        .offset:         152
        .size:           8
        .value_kind:     global_buffer
    .group_segment_fixed_size: 126720
    .kernarg_segment_align: 8
    .kernarg_segment_size: 160
    .language:       OpenCL C
    .language_version:
      - 2
      - 0
    .max_flat_workgroup_size: 512
    .name:           _Z7k_layerILi0EEvPKDF16_S1_PKfS3_S3_S3_S3_S3_S1_S1_S1_S1_S3_S3_PKhS5_PDF16_S6_PfS7_
    .private_segment_fixed_size: 0
    .sgpr_count:     50
    .sgpr_spill_count: 0
    .symbol:         _Z7k_layerILi0EEvPKDF16_S1_PKfS3_S3_S3_S3_S3_S1_S1_S1_S1_S3_S3_PKhS5_PDF16_S6_PfS7_.kd
    .uniform_work_group_size: 1
    .uses_dynamic_stack: false
    .vgpr_count:     256
    .vgpr_spill_count: 0
    .wavefront_size: 64
